# speedup vs baseline: 1.0417x; 1.0053x over previous
_Z16bilateral_kernelPKfS0_Pf:
	s_load_dwordx2 s[4:5], s[0:1], 0x0
	s_load_dwordx2 s[8:9], s[0:1], 0x10
	s_and_b32 s0, s2, 7
	s_mulk_i32 s0, 0x60
	s_lshr_b32 s1, s2, 3
	s_add_i32 s1, s0, s1
	s_lshr_b32 s0, s1, 6
	s_lshl_b32 s1, s1, 3
	s_and_b32 s10, s1, 0x1c0
	s_lshl_b32 s1, s2, 3
	s_nop 0
	s_and_b32 s11, s1, 0x1c0
	s_mov_b32 s1, 0
	s_lshl_b64 s[2:3], s[0:1], 20
	s_mov_b32 s20, 0xc05dfbe6
	s_mov_b32 s21, 0xc05dfbe6
	s_mov_b32 s22, 0xc0a8390e
	s_mov_b32 s23, 0xc0a8390e
	s_mov_b32 s24, 0xc08211a7
	s_mov_b32 s25, 0xc08211a7
	s_mov_b32 s26, 0xc0bb4cc1
	s_mov_b32 s27, 0xc0bb4cc1
	s_mov_b32 s28, 0xc0f487dc
	s_mov_b32 s29, 0xc0f487dc
	s_mov_b32 s30, 0x3e0bd796
	s_mov_b32 s31, 0x3e0bd796
	s_mov_b32 s32, 0x3f45a90c
	s_mov_b32 s33, 0x3f45a90c
	s_mov_b32 s34, 0x3fa5c782
	s_mov_b32 s35, 0x3fa5c782
	v_and_b32_e32 v118, 15, v0
	v_lshrrev_b32_e32 v115, 2, v0
	v_lshl_or_b32 v113, v118, 2, s11
	v_and_or_b32 v117, v115, 60, s10
	v_min_u32_e32 v116, 0x1fa, v113
	v_sub_u32_e64 v115, v113, 2 clamp
	v_add_u32_e32 v116, 4, v116
	s_nop 0
	v_cmp_eq_u32_e64 s[16:17], 0, v118
	v_cmp_eq_u32_e32 vcc, 15, v118
	s_nop 1
	v_cndmask_b32_e64 v115, v116, v115, s[16:17]
	s_or_b64 vcc, s[16:17], vcc
	v_lshlrev_b32_e32 v115, 2, v115
	v_mov_b32_e32 v116, 0x7ff00000
	s_nop 0
	v_cndmask_b32_e32 v112, v116, v115, vcc
	s_movk_i32 s18, 0x1fc
	v_cmp_eq_u32_e32 vcc, 0, v113
	v_cmp_eq_u32_e64 s[16:17], s18, v113
	v_lshlrev_b32_e32 v113, 2, v113
	s_waitcnt lgkmcnt(0)
	s_add_u32 s4, s4, s2
	s_addc_u32 s5, s5, s3
	s_and_b32 s5, s5, 0xffff
	s_mov_b32 s6, 0x100000
	s_mov_b32 s7, 0x20000
	s_add_u32 s12, s8, s2
	s_addc_u32 s13, s9, s3
	s_and_b32 s13, s13, 0xffff
	s_mov_b32 s14, 0x100000
	s_mov_b32 s15, 0x20000
	v_sub_u32_e64 v115, v117, 2 clamp
	v_lshlrev_b32_e32 v115, 11, v115
	v_add_u32_e32 v116, v115, v112
	v_add_u32_e32 v115, v115, v113
	s_nop 0
	buffer_load_dwordx2 v[0:1], v116, s[4:7], 0 offen nt
	buffer_load_dwordx2 v[6:7], v116, s[4:7], 0 offen nt
	buffer_load_dwordx4 v[2:5], v115, s[4:7], 0 offen nt
	v_sub_u32_e64 v115, v117, 1 clamp
	v_lshlrev_b32_e32 v115, 11, v115
	v_add_u32_e32 v116, v115, v112
	v_add_u32_e32 v115, v115, v113
	s_nop 0
	buffer_load_dwordx2 v[8:9], v116, s[4:7], 0 offen nt
	buffer_load_dwordx2 v[14:15], v116, s[4:7], 0 offen nt
	buffer_load_dwordx4 v[10:13], v115, s[4:7], 0 offen nt
	v_lshlrev_b32_e32 v115, 11, v117
	v_add_u32_e32 v116, v115, v112
	v_add_u32_e32 v114, v115, v113
	s_nop 0
	v_add_u32_e32 v119, 0x1000, v114
	buffer_load_dwordx2 v[16:17], v116, s[4:7], 0 offen nt
	buffer_load_dwordx2 v[22:23], v116, s[4:7], 0 offen nt
	buffer_load_dwordx4 v[18:21], v114, s[4:7], 0 offen nt
	v_lshlrev_b32_e32 v115, 11, v117
	s_nop 0
	v_add_u32_e32 v115, 0x800, v115
	v_add_u32_e32 v116, v115, v112
	v_add_u32_e32 v115, v115, v113
	buffer_load_dwordx2 v[24:25], v116, s[4:7], 0 offen nt
	buffer_load_dwordx2 v[30:31], v116, s[4:7], 0 offen nt
	buffer_load_dwordx4 v[26:29], v115, s[4:7], 0 offen nt
	v_lshlrev_b32_e32 v115, 11, v117
	s_nop 0
	v_add_u32_e32 v115, 0x1000, v115
	v_add_u32_e32 v116, v115, v112
	v_add_u32_e32 v115, v115, v113
	buffer_load_dwordx2 v[32:33], v116, s[4:7], 0 offen nt
	buffer_load_dwordx2 v[38:39], v116, s[4:7], 0 offen nt
	buffer_load_dwordx4 v[34:37], v115, s[4:7], 0 offen nt
	v_lshlrev_b32_e32 v115, 11, v117
	s_nop 0
	v_add_u32_e32 v115, 0x1800, v115
	v_add_u32_e32 v116, v115, v112
	v_add_u32_e32 v115, v115, v113
	buffer_load_dwordx2 v[40:41], v116, s[4:7], 0 offen nt
	buffer_load_dwordx2 v[46:47], v116, s[4:7], 0 offen nt
	buffer_load_dwordx4 v[42:45], v115, s[4:7], 0 offen nt
	v_min_u32_e32 v115, 0x1fb, v117
	v_lshlrev_b32_e32 v115, 11, v115
	s_nop 0
	v_add_u32_e32 v115, 0x2000, v115
	v_add_u32_e32 v116, v115, v112
	v_add_u32_e32 v115, v115, v113
	buffer_load_dwordx2 v[48:49], v116, s[4:7], 0 offen nt
	buffer_load_dwordx2 v[54:55], v116, s[4:7], 0 offen nt
	buffer_load_dwordx4 v[50:53], v115, s[4:7], 0 offen nt
	v_min_u32_e32 v115, 0x1fa, v117
	v_lshlrev_b32_e32 v115, 11, v115
	s_nop 0
	v_add_u32_e32 v115, 0x2800, v115
	v_add_u32_e32 v116, v115, v112
	v_add_u32_e32 v115, v115, v113
	buffer_load_dwordx2 v[56:57], v116, s[4:7], 0 offen nt
	buffer_load_dwordx2 v[62:63], v116, s[4:7], 0 offen nt
	buffer_load_dwordx4 v[58:61], v115, s[4:7], 0 offen nt
	s_waitcnt vmcnt(21)
	s_nop 0
	v_mov_b32_dpp v0, v4 row_shr:1 row_mask:0xf bank_mask:0xf
	v_mov_b32_dpp v1, v5 row_shr:1 row_mask:0xf bank_mask:0xf
	v_mov_b32_dpp v6, v2 row_shl:1 row_mask:0xf bank_mask:0xf
	v_mov_b32_dpp v7, v3 row_shl:1 row_mask:0xf bank_mask:0xf
	v_pk_mul_f32 v[2:3], v[2:3], s[32:33]
	v_pk_mul_f32 v[4:5], v[4:5], s[32:33]
	v_cndmask_b32_e64 v1, v1, v0, vcc
	v_cndmask_b32_e64 v6, v6, v7, s[16:17]
	v_pk_mul_f32 v[0:1], v[0:1], s[32:33]
	v_pk_mul_f32 v[6:7], v[6:7], s[32:33]
	s_waitcnt vmcnt(18)
	s_nop 0
	v_mov_b32_dpp v8, v12 row_shr:1 row_mask:0xf bank_mask:0xf
	v_mov_b32_dpp v9, v13 row_shr:1 row_mask:0xf bank_mask:0xf
	v_mov_b32_dpp v14, v10 row_shl:1 row_mask:0xf bank_mask:0xf
	v_mov_b32_dpp v15, v11 row_shl:1 row_mask:0xf bank_mask:0xf
	v_pk_mul_f32 v[10:11], v[10:11], s[32:33]
	v_pk_mul_f32 v[12:13], v[12:13], s[32:33]
	v_cndmask_b32_e64 v9, v9, v8, vcc
	v_cndmask_b32_e64 v14, v14, v15, s[16:17]
	v_pk_mul_f32 v[8:9], v[8:9], s[32:33]
	v_pk_mul_f32 v[14:15], v[14:15], s[32:33]
	s_waitcnt vmcnt(15)
	s_nop 0
	v_mov_b32_dpp v16, v20 row_shr:1 row_mask:0xf bank_mask:0xf
	v_mov_b32_dpp v17, v21 row_shr:1 row_mask:0xf bank_mask:0xf
	v_mov_b32_dpp v22, v18 row_shl:1 row_mask:0xf bank_mask:0xf
	v_mov_b32_dpp v23, v19 row_shl:1 row_mask:0xf bank_mask:0xf
	v_pk_mul_f32 v[18:19], v[18:19], s[32:33]
	v_pk_mul_f32 v[20:21], v[20:21], s[32:33]
	v_cndmask_b32_e64 v17, v17, v16, vcc
	v_cndmask_b32_e64 v22, v22, v23, s[16:17]
	v_pk_mul_f32 v[68:69], v[18:19], s[30:31]
	v_pk_mul_f32 v[70:71], v[20:21], s[30:31]
	v_pk_mul_f32 v[16:17], v[16:17], s[32:33]
	v_pk_mul_f32 v[22:23], v[22:23], s[32:33]
	v_mov_b32_e32 v64, s30
	v_mov_b32_e32 v65, s30
	v_mov_b32_e32 v66, s30
	v_mov_b32_e32 v67, s30
	s_setprio 3
	s_nop 0
	v_pk_add_f32 v[96:97], v[18:19], v[0:1] neg_lo:[0,1] neg_hi:[0,1]
	v_pk_add_f32 v[98:99], v[18:19], v[2:3] neg_lo:[0,1] neg_hi:[0,1]
	v_pk_add_f32 v[100:101], v[20:21], v[2:3] neg_lo:[0,1] neg_hi:[0,1]
	v_pk_add_f32 v[102:103], v[18:19], v[4:5] neg_lo:[0,1] neg_hi:[0,1]
	v_pk_fma_f32 v[96:97], v[96:97], v[96:97], s[28:29] neg_lo:[1,0,0] neg_hi:[1,0,0]
	v_pk_fma_f32 v[98:99], v[98:99], v[98:99], s[22:23] neg_lo:[1,0,0] neg_hi:[1,0,0]
	v_pk_fma_f32 v[100:101], v[100:101], v[100:101], s[28:29] neg_lo:[1,0,0] neg_hi:[1,0,0]
	v_pk_fma_f32 v[102:103], v[102:103], v[102:103], s[28:29] neg_lo:[1,0,0] neg_hi:[1,0,0]
	v_exp_f32_e32 v96, v96
	v_exp_f32_e32 v97, v97
	v_exp_f32_e32 v98, v98
	v_exp_f32_e32 v99, v99
	v_exp_f32_e32 v100, v100
	v_exp_f32_e32 v101, v101
	v_exp_f32_e32 v102, v102
	v_exp_f32_e32 v103, v103
	v_pk_add_f32 v[104:105], v[20:21], v[4:5] neg_lo:[0,1] neg_hi:[0,1]
	v_pk_add_f32 v[106:107], v[20:21], v[6:7] neg_lo:[0,1] neg_hi:[0,1]
	v_pk_add_f32 v[108:109], v[18:19], v[2:3] op_sel:[1,0] op_sel_hi:[0,1] neg_lo:[0,1] neg_hi:[0,1]
	v_pk_add_f32 v[110:111], v[20:21], v[4:5] op_sel:[1,0] op_sel_hi:[0,1] neg_lo:[0,1] neg_hi:[0,1]
	v_pk_fma_f32 v[104:105], v[104:105], v[104:105], s[22:23] neg_lo:[1,0,0] neg_hi:[1,0,0]
	v_pk_fma_f32 v[106:107], v[106:107], v[106:107], s[28:29] neg_lo:[1,0,0] neg_hi:[1,0,0]
	v_pk_fma_f32 v[108:109], v[108:109], v[108:109], s[26:27] neg_lo:[1,0,0] neg_hi:[1,0,0]
	v_pk_fma_f32 v[110:111], v[110:111], v[110:111], s[26:27] neg_lo:[1,0,0] neg_hi:[1,0,0]
	v_exp_f32_e32 v104, v104
	v_exp_f32_e32 v105, v105
	v_exp_f32_e32 v106, v106
	v_exp_f32_e32 v107, v107
	v_exp_f32_e32 v108, v108
	v_exp_f32_e32 v109, v109
	v_exp_f32_e32 v110, v110
	v_exp_f32_e32 v111, v111
	v_pk_add_f32 v[64:65], v[64:65], v[96:97]
	v_pk_fma_f32 v[68:69], v[96:97], v[0:1], v[68:69]
	v_pk_add_f32 v[66:67], v[66:67], v[100:101]
	v_pk_add_f32 v[64:65], v[64:65], v[98:99]
	v_pk_fma_f32 v[68:69], v[98:99], v[2:3], v[68:69]
	v_pk_fma_f32 v[70:71], v[100:101], v[2:3], v[70:71]
	v_pk_add_f32 v[64:65], v[64:65], v[102:103]
	v_pk_fma_f32 v[68:69], v[102:103], v[4:5], v[68:69]
	v_pk_add_f32 v[96:97], v[18:19], v[8:9] neg_lo:[0,1] neg_hi:[0,1]
	v_pk_add_f32 v[98:99], v[18:19], v[10:11] neg_lo:[0,1] neg_hi:[0,1]
	v_pk_add_f32 v[100:101], v[20:21], v[10:11] neg_lo:[0,1] neg_hi:[0,1]
	v_pk_add_f32 v[102:103], v[18:19], v[12:13] neg_lo:[0,1] neg_hi:[0,1]
	v_pk_fma_f32 v[96:97], v[96:97], v[96:97], s[26:27] neg_lo:[1,0,0] neg_hi:[1,0,0]
	v_pk_fma_f32 v[98:99], v[98:99], v[98:99], s[20:21] neg_lo:[1,0,0] neg_hi:[1,0,0]
	v_pk_fma_f32 v[100:101], v[100:101], v[100:101], s[26:27] neg_lo:[1,0,0] neg_hi:[1,0,0]
	v_pk_fma_f32 v[102:103], v[102:103], v[102:103], s[26:27] neg_lo:[1,0,0] neg_hi:[1,0,0]
	v_exp_f32_e32 v96, v96
	v_exp_f32_e32 v97, v97
	v_exp_f32_e32 v98, v98
	v_exp_f32_e32 v99, v99
	v_exp_f32_e32 v100, v100
	v_exp_f32_e32 v101, v101
	v_exp_f32_e32 v102, v102
	v_exp_f32_e32 v103, v103
	v_pk_add_f32 v[66:67], v[66:67], v[104:105]
	v_pk_fma_f32 v[70:71], v[104:105], v[4:5], v[70:71]
	v_pk_add_f32 v[64:65], v[64:65], v[108:109] op_sel:[0,1] op_sel_hi:[1,0]
	v_pk_add_f32 v[66:67], v[66:67], v[106:107]
	v_pk_fma_f32 v[70:71], v[106:107], v[6:7], v[70:71]
	v_pk_fma_f32 v[68:69], v[108:109], v[2:3], v[68:69] op_sel:[1,1,0] op_sel_hi:[0,0,1]
	v_pk_add_f32 v[66:67], v[66:67], v[110:111] op_sel:[0,1] op_sel_hi:[1,0]
	v_pk_fma_f32 v[70:71], v[110:111], v[4:5], v[70:71] op_sel:[1,1,0] op_sel_hi:[0,0,1]
	v_pk_add_f32 v[104:105], v[20:21], v[12:13] neg_lo:[0,1] neg_hi:[0,1]
	v_pk_add_f32 v[106:107], v[20:21], v[14:15] neg_lo:[0,1] neg_hi:[0,1]
	v_pk_add_f32 v[108:109], v[18:19], v[10:11] op_sel:[1,0] op_sel_hi:[0,1] neg_lo:[0,1] neg_hi:[0,1]
	v_pk_add_f32 v[110:111], v[20:21], v[12:13] op_sel:[1,0] op_sel_hi:[0,1] neg_lo:[0,1] neg_hi:[0,1]
	v_pk_fma_f32 v[104:105], v[104:105], v[104:105], s[20:21] neg_lo:[1,0,0] neg_hi:[1,0,0]
	v_pk_fma_f32 v[106:107], v[106:107], v[106:107], s[26:27] neg_lo:[1,0,0] neg_hi:[1,0,0]
	v_pk_fma_f32 v[108:109], v[108:109], v[108:109], s[24:25] neg_lo:[1,0,0] neg_hi:[1,0,0]
	v_pk_fma_f32 v[110:111], v[110:111], v[110:111], s[24:25] neg_lo:[1,0,0] neg_hi:[1,0,0]
	v_exp_f32_e32 v104, v104
	v_exp_f32_e32 v105, v105
	v_exp_f32_e32 v106, v106
	v_exp_f32_e32 v107, v107
	v_exp_f32_e32 v108, v108
	v_exp_f32_e32 v109, v109
	v_exp_f32_e32 v110, v110
	v_exp_f32_e32 v111, v111
	v_pk_add_f32 v[64:65], v[64:65], v[96:97]
	v_pk_fma_f32 v[68:69], v[96:97], v[8:9], v[68:69]
	v_pk_add_f32 v[66:67], v[66:67], v[100:101]
	v_pk_add_f32 v[64:65], v[64:65], v[98:99]
	v_pk_fma_f32 v[68:69], v[98:99], v[10:11], v[68:69]
	v_pk_fma_f32 v[70:71], v[100:101], v[10:11], v[70:71]
	v_pk_add_f32 v[64:65], v[64:65], v[102:103]
	v_pk_fma_f32 v[68:69], v[102:103], v[12:13], v[68:69]
	v_pk_add_f32 v[96:97], v[18:19], v[16:17] neg_lo:[0,1] neg_hi:[0,1]
	v_pk_add_f32 v[98:99], v[20:21], v[18:19] neg_lo:[0,1] neg_hi:[0,1]
	v_pk_add_f32 v[100:101], v[22:23], v[20:21] neg_lo:[0,1] neg_hi:[0,1]
	v_pk_fma_f32 v[96:97], v[96:97], v[96:97], s[22:23] neg_lo:[1,0,0] neg_hi:[1,0,0]
	v_pk_fma_f32 v[98:99], v[98:99], v[98:99], s[22:23] neg_lo:[1,0,0] neg_hi:[1,0,0]
	v_pk_fma_f32 v[100:101], v[100:101], v[100:101], s[22:23] neg_lo:[1,0,0] neg_hi:[1,0,0]
	v_exp_f32_e32 v96, v96
	v_exp_f32_e32 v97, v97
	v_exp_f32_e32 v98, v98
	v_exp_f32_e32 v99, v99
	v_exp_f32_e32 v100, v100
	v_exp_f32_e32 v101, v101
	v_pk_add_f32 v[66:67], v[66:67], v[104:105]
	v_pk_fma_f32 v[70:71], v[104:105], v[12:13], v[70:71]
	v_pk_add_f32 v[64:65], v[64:65], v[108:109] op_sel:[0,1] op_sel_hi:[1,0]
	v_pk_add_f32 v[66:67], v[66:67], v[106:107]
	v_pk_fma_f32 v[70:71], v[106:107], v[14:15], v[70:71]
	v_pk_fma_f32 v[68:69], v[108:109], v[10:11], v[68:69] op_sel:[1,1,0] op_sel_hi:[0,0,1]
	v_pk_add_f32 v[66:67], v[66:67], v[110:111] op_sel:[0,1] op_sel_hi:[1,0]
	v_pk_fma_f32 v[70:71], v[110:111], v[12:13], v[70:71] op_sel:[1,1,0] op_sel_hi:[0,0,1]
	v_sub_f32_e32 v104, v18, v1
	v_sub_f32_e32 v106, v20, v3
	v_sub_f32_e32 v108, v19, v4
	v_sub_f32_e32 v110, v21, v6
	v_sub_f32_e32 v105, v18, v9
	v_sub_f32_e32 v107, v20, v11
	v_sub_f32_e32 v109, v19, v12
	v_sub_f32_e32 v111, v21, v14
	v_fma_f32 v104, -v104, v104, s26
	v_fma_f32 v106, -v106, v106, s26
	v_fma_f32 v108, -v108, v108, s26
	v_fma_f32 v110, -v110, v110, s26
	v_fma_f32 v105, -v105, v105, s24
	v_fma_f32 v107, -v107, v107, s24
	v_fma_f32 v109, -v109, v109, s24
	v_fma_f32 v111, -v111, v111, s24
	v_exp_f32_e32 v104, v104
	v_exp_f32_e32 v106, v106
	v_exp_f32_e32 v108, v108
	v_exp_f32_e32 v110, v110
	v_exp_f32_e32 v105, v105
	v_exp_f32_e32 v107, v107
	v_exp_f32_e32 v109, v109
	v_exp_f32_e32 v111, v111
	v_pk_add_f32 v[64:65], v[64:65], v[96:97]
	v_pk_fma_f32 v[68:69], v[96:97], v[16:17], v[68:69]
	v_pk_add_f32 v[66:67], v[66:67], v[98:99]
	v_pk_add_f32 v[64:65], v[64:65], v[98:99]
	v_pk_fma_f32 v[68:69], v[98:99], v[20:21], v[68:69]
	v_pk_fma_f32 v[70:71], v[98:99], v[18:19], v[70:71]
	v_pk_add_f32 v[66:67], v[66:67], v[100:101]
	v_pk_fma_f32 v[70:71], v[100:101], v[22:23], v[70:71]
	v_sub_f32_e32 v100, v18, v17
	v_sub_f32_e32 v96, v19, v18
	v_sub_f32_e32 v102, v20, v19
	v_sub_f32_e32 v98, v21, v20
	v_sub_f32_e32 v97, v22, v21
	s_nop 0
	v_fma_f32 v100, -v100, v100, s20
	v_fma_f32 v96, -v96, v96, s20
	v_fma_f32 v102, -v102, v102, s20
	v_fma_f32 v98, -v98, v98, s20
	v_fma_f32 v97, -v97, v97, s20
	v_exp_f32_e32 v100, v100
	v_exp_f32_e32 v96, v96
	v_exp_f32_e32 v102, v102
	v_exp_f32_e32 v98, v98
	v_exp_f32_e32 v97, v97
	v_add_f32_e32 v64, v64, v104
	v_fmac_f32_e32 v68, v104, v1
	v_add_f32_e32 v66, v66, v106
	v_fmac_f32_e32 v70, v106, v3
	v_add_f32_e32 v65, v65, v108
	v_fmac_f32_e32 v69, v108, v4
	v_add_f32_e32 v67, v67, v110
	v_fmac_f32_e32 v71, v110, v6
	v_add_f32_e32 v64, v64, v105
	v_fmac_f32_e32 v68, v105, v9
	v_add_f32_e32 v66, v66, v107
	v_fmac_f32_e32 v70, v107, v11
	v_add_f32_e32 v65, v65, v109
	v_fmac_f32_e32 v69, v109, v12
	v_add_f32_e32 v67, v67, v111
	v_fmac_f32_e32 v71, v111, v14
	v_add_f32_e32 v64, v64, v100
	v_fmac_f32_e32 v68, v100, v17
	v_add_f32_e32 v65, v65, v102
	v_fmac_f32_e32 v69, v102, v20
	v_add_f32_e32 v66, v66, v102
	v_fmac_f32_e32 v70, v102, v19
	v_add_f32_e32 v67, v67, v97
	v_fmac_f32_e32 v71, v97, v22
	s_nop 0
	v_pk_add_f32 v[64:65], v[64:65], v[96:97] op_sel_hi:[1,0]
	v_pk_fma_f32 v[68:69], v[96:97], v[18:19], v[68:69] op_sel:[0,1,0] op_sel_hi:[0,0,1]
	v_pk_add_f32 v[66:67], v[66:67], v[98:99] op_sel_hi:[1,0]
	v_pk_fma_f32 v[70:71], v[98:99], v[20:21], v[70:71] op_sel:[0,1,0] op_sel_hi:[0,0,1]
	s_waitcnt vmcnt(12)
	s_nop 0
	v_mov_b32_dpp v24, v28 row_shr:1 row_mask:0xf bank_mask:0xf
	v_mov_b32_dpp v25, v29 row_shr:1 row_mask:0xf bank_mask:0xf
	v_mov_b32_dpp v30, v26 row_shl:1 row_mask:0xf bank_mask:0xf
	v_mov_b32_dpp v31, v27 row_shl:1 row_mask:0xf bank_mask:0xf
	v_pk_mul_f32 v[26:27], v[26:27], s[32:33]
	v_pk_mul_f32 v[28:29], v[28:29], s[32:33]
	v_cndmask_b32_e64 v25, v25, v24, vcc
	v_cndmask_b32_e64 v30, v30, v31, s[16:17]
	v_pk_mul_f32 v[76:77], v[26:27], s[30:31]
	v_pk_mul_f32 v[78:79], v[28:29], s[30:31]
	v_pk_mul_f32 v[24:25], v[24:25], s[32:33]
	v_pk_mul_f32 v[30:31], v[30:31], s[32:33]
	v_mov_b32_e32 v72, s30
	v_mov_b32_e32 v73, s30
	v_mov_b32_e32 v74, s30
	v_mov_b32_e32 v75, s30
	s_setprio 3
	s_nop 0
	v_pk_add_f32 v[96:97], v[26:27], v[8:9] neg_lo:[0,1] neg_hi:[0,1]
	v_pk_add_f32 v[98:99], v[26:27], v[10:11] neg_lo:[0,1] neg_hi:[0,1]
	v_pk_add_f32 v[100:101], v[28:29], v[10:11] neg_lo:[0,1] neg_hi:[0,1]
	v_pk_add_f32 v[102:103], v[26:27], v[12:13] neg_lo:[0,1] neg_hi:[0,1]
	v_pk_fma_f32 v[96:97], v[96:97], v[96:97], s[28:29] neg_lo:[1,0,0] neg_hi:[1,0,0]
	v_pk_fma_f32 v[98:99], v[98:99], v[98:99], s[22:23] neg_lo:[1,0,0] neg_hi:[1,0,0]
	v_pk_fma_f32 v[100:101], v[100:101], v[100:101], s[28:29] neg_lo:[1,0,0] neg_hi:[1,0,0]
	v_pk_fma_f32 v[102:103], v[102:103], v[102:103], s[28:29] neg_lo:[1,0,0] neg_hi:[1,0,0]
	v_exp_f32_e32 v96, v96
	v_exp_f32_e32 v97, v97
	v_exp_f32_e32 v98, v98
	v_exp_f32_e32 v99, v99
	v_exp_f32_e32 v100, v100
	v_exp_f32_e32 v101, v101
	v_exp_f32_e32 v102, v102
	v_exp_f32_e32 v103, v103
	v_pk_add_f32 v[104:105], v[28:29], v[12:13] neg_lo:[0,1] neg_hi:[0,1]
	v_pk_add_f32 v[106:107], v[28:29], v[14:15] neg_lo:[0,1] neg_hi:[0,1]
	v_pk_add_f32 v[108:109], v[26:27], v[10:11] op_sel:[1,0] op_sel_hi:[0,1] neg_lo:[0,1] neg_hi:[0,1]
	v_pk_add_f32 v[110:111], v[28:29], v[12:13] op_sel:[1,0] op_sel_hi:[0,1] neg_lo:[0,1] neg_hi:[0,1]
	v_pk_fma_f32 v[104:105], v[104:105], v[104:105], s[22:23] neg_lo:[1,0,0] neg_hi:[1,0,0]
	v_pk_fma_f32 v[106:107], v[106:107], v[106:107], s[28:29] neg_lo:[1,0,0] neg_hi:[1,0,0]
	v_pk_fma_f32 v[108:109], v[108:109], v[108:109], s[26:27] neg_lo:[1,0,0] neg_hi:[1,0,0]
	v_pk_fma_f32 v[110:111], v[110:111], v[110:111], s[26:27] neg_lo:[1,0,0] neg_hi:[1,0,0]
	v_exp_f32_e32 v104, v104
	v_exp_f32_e32 v105, v105
	v_exp_f32_e32 v106, v106
	v_exp_f32_e32 v107, v107
	v_exp_f32_e32 v108, v108
	v_exp_f32_e32 v109, v109
	v_exp_f32_e32 v110, v110
	v_exp_f32_e32 v111, v111
	v_pk_add_f32 v[72:73], v[72:73], v[96:97]
	v_pk_fma_f32 v[76:77], v[96:97], v[8:9], v[76:77]
	v_pk_add_f32 v[74:75], v[74:75], v[100:101]
	v_pk_add_f32 v[72:73], v[72:73], v[98:99]
	v_pk_fma_f32 v[76:77], v[98:99], v[10:11], v[76:77]
	v_pk_fma_f32 v[78:79], v[100:101], v[10:11], v[78:79]
	v_pk_add_f32 v[72:73], v[72:73], v[102:103]
	v_pk_fma_f32 v[76:77], v[102:103], v[12:13], v[76:77]
	v_pk_add_f32 v[96:97], v[26:27], v[16:17] neg_lo:[0,1] neg_hi:[0,1]
	v_pk_add_f32 v[98:99], v[24:25], v[18:19] neg_lo:[0,1] neg_hi:[0,1]
	v_pk_add_f32 v[100:101], v[26:27], v[18:19] neg_lo:[0,1] neg_hi:[0,1]
	v_pk_add_f32 v[102:103], v[28:29], v[18:19] neg_lo:[0,1] neg_hi:[0,1]
	v_pk_fma_f32 v[96:97], v[96:97], v[96:97], s[26:27] neg_lo:[1,0,0] neg_hi:[1,0,0]
	v_pk_fma_f32 v[98:99], v[98:99], v[98:99], s[26:27] neg_lo:[1,0,0] neg_hi:[1,0,0]
	v_pk_fma_f32 v[100:101], v[100:101], v[100:101], s[20:21] neg_lo:[1,0,0] neg_hi:[1,0,0]
	v_pk_fma_f32 v[102:103], v[102:103], v[102:103], s[26:27] neg_lo:[1,0,0] neg_hi:[1,0,0]
	v_exp_f32_e32 v96, v96
	v_exp_f32_e32 v97, v97
	v_exp_f32_e32 v98, v98
	v_exp_f32_e32 v99, v99
	v_exp_f32_e32 v100, v100
	v_exp_f32_e32 v101, v101
	v_exp_f32_e32 v102, v102
	v_exp_f32_e32 v103, v103
	v_pk_add_f32 v[74:75], v[74:75], v[104:105]
	v_pk_fma_f32 v[78:79], v[104:105], v[12:13], v[78:79]
	v_pk_add_f32 v[72:73], v[72:73], v[108:109] op_sel:[0,1] op_sel_hi:[1,0]
	v_pk_add_f32 v[74:75], v[74:75], v[106:107]
	v_pk_fma_f32 v[78:79], v[106:107], v[14:15], v[78:79]
	v_pk_fma_f32 v[76:77], v[108:109], v[10:11], v[76:77] op_sel:[1,1,0] op_sel_hi:[0,0,1]
	v_pk_add_f32 v[74:75], v[74:75], v[110:111] op_sel:[0,1] op_sel_hi:[1,0]
	v_pk_fma_f32 v[78:79], v[110:111], v[12:13], v[78:79] op_sel:[1,1,0] op_sel_hi:[0,0,1]
	v_pk_add_f32 v[104:105], v[26:27], v[20:21] neg_lo:[0,1] neg_hi:[0,1]
	v_pk_add_f32 v[106:107], v[28:29], v[20:21] neg_lo:[0,1] neg_hi:[0,1]
	v_pk_add_f32 v[108:109], v[30:31], v[20:21] neg_lo:[0,1] neg_hi:[0,1]
	v_pk_add_f32 v[110:111], v[28:29], v[22:23] neg_lo:[0,1] neg_hi:[0,1]
	v_pk_fma_f32 v[104:105], v[104:105], v[104:105], s[26:27] neg_lo:[1,0,0] neg_hi:[1,0,0]
	v_pk_fma_f32 v[106:107], v[106:107], v[106:107], s[20:21] neg_lo:[1,0,0] neg_hi:[1,0,0]
	v_pk_fma_f32 v[108:109], v[108:109], v[108:109], s[26:27] neg_lo:[1,0,0] neg_hi:[1,0,0]
	v_pk_fma_f32 v[110:111], v[110:111], v[110:111], s[26:27] neg_lo:[1,0,0] neg_hi:[1,0,0]
	v_exp_f32_e32 v104, v104
	v_exp_f32_e32 v105, v105
	v_exp_f32_e32 v106, v106
	v_exp_f32_e32 v107, v107
	v_exp_f32_e32 v108, v108
	v_exp_f32_e32 v109, v109
	v_exp_f32_e32 v110, v110
	v_exp_f32_e32 v111, v111
	v_pk_add_f32 v[72:73], v[72:73], v[96:97]
	v_pk_fma_f32 v[76:77], v[96:97], v[16:17], v[76:77]
	v_pk_add_f32 v[64:65], v[64:65], v[98:99]
	v_pk_fma_f32 v[68:69], v[98:99], v[24:25], v[68:69]
	v_pk_add_f32 v[72:73], v[72:73], v[100:101]
	v_pk_add_f32 v[64:65], v[64:65], v[100:101]
	v_pk_fma_f32 v[68:69], v[100:101], v[26:27], v[68:69]
	v_pk_fma_f32 v[76:77], v[100:101], v[18:19], v[76:77]
	v_pk_add_f32 v[64:65], v[64:65], v[102:103]
	v_pk_fma_f32 v[68:69], v[102:103], v[28:29], v[68:69]
	v_pk_add_f32 v[74:75], v[74:75], v[102:103]
	v_pk_fma_f32 v[78:79], v[102:103], v[18:19], v[78:79]
	v_pk_add_f32 v[96:97], v[26:27], v[18:19] op_sel:[1,0] op_sel_hi:[0,1] neg_lo:[0,1] neg_hi:[0,1]
	v_pk_add_f32 v[98:99], v[28:29], v[20:21] op_sel:[1,0] op_sel_hi:[0,1] neg_lo:[0,1] neg_hi:[0,1]
	v_pk_add_f32 v[100:101], v[26:27], v[24:25] neg_lo:[0,1] neg_hi:[0,1]
	v_pk_add_f32 v[102:103], v[28:29], v[26:27] neg_lo:[0,1] neg_hi:[0,1]
	v_pk_fma_f32 v[96:97], v[96:97], v[96:97], s[24:25] neg_lo:[1,0,0] neg_hi:[1,0,0]
	v_pk_fma_f32 v[98:99], v[98:99], v[98:99], s[24:25] neg_lo:[1,0,0] neg_hi:[1,0,0]
	v_pk_fma_f32 v[100:101], v[100:101], v[100:101], s[22:23] neg_lo:[1,0,0] neg_hi:[1,0,0]
	v_pk_fma_f32 v[102:103], v[102:103], v[102:103], s[22:23] neg_lo:[1,0,0] neg_hi:[1,0,0]
	v_exp_f32_e32 v96, v96
	v_exp_f32_e32 v97, v97
	v_exp_f32_e32 v98, v98
	v_exp_f32_e32 v99, v99
	v_exp_f32_e32 v100, v100
	v_exp_f32_e32 v101, v101
	v_exp_f32_e32 v102, v102
	v_exp_f32_e32 v103, v103
	v_pk_add_f32 v[66:67], v[66:67], v[104:105]
	v_pk_fma_f32 v[70:71], v[104:105], v[26:27], v[70:71]
	v_pk_add_f32 v[72:73], v[72:73], v[104:105]
	v_pk_fma_f32 v[76:77], v[104:105], v[20:21], v[76:77]
	v_pk_add_f32 v[66:67], v[66:67], v[106:107]
	v_pk_fma_f32 v[70:71], v[106:107], v[28:29], v[70:71]
	v_pk_add_f32 v[74:75], v[74:75], v[106:107]
	v_pk_fma_f32 v[78:79], v[106:107], v[20:21], v[78:79]
	v_pk_add_f32 v[66:67], v[66:67], v[108:109]
	v_pk_fma_f32 v[70:71], v[108:109], v[30:31], v[70:71]
	v_pk_add_f32 v[74:75], v[74:75], v[110:111]
	v_pk_fma_f32 v[78:79], v[110:111], v[22:23], v[78:79]
	v_pk_add_f32 v[104:105], v[30:31], v[28:29] neg_lo:[0,1] neg_hi:[0,1]
	v_pk_fma_f32 v[104:105], v[104:105], v[104:105], s[22:23] neg_lo:[1,0,0] neg_hi:[1,0,0]
	s_nop 0
	v_exp_f32_e32 v104, v104
	v_exp_f32_e32 v105, v105
	s_nop 0
	v_pk_add_f32 v[64:65], v[64:65], v[96:97]
	v_pk_fma_f32 v[68:69], v[96:97], v[26:27], v[68:69] op_sel:[0,1,0] op_sel_hi:[1,0,1]
	v_pk_add_f32 v[72:73], v[72:73], v[96:97] op_sel:[0,1] op_sel_hi:[1,0]
	v_pk_fma_f32 v[76:77], v[96:97], v[18:19], v[76:77] op_sel:[1,1,0] op_sel_hi:[0,0,1]
	v_pk_add_f32 v[66:67], v[66:67], v[98:99]
	v_pk_fma_f32 v[70:71], v[98:99], v[28:29], v[70:71] op_sel:[0,1,0] op_sel_hi:[1,0,1]
	v_pk_add_f32 v[74:75], v[74:75], v[98:99] op_sel:[0,1] op_sel_hi:[1,0]
	v_pk_fma_f32 v[78:79], v[98:99], v[20:21], v[78:79] op_sel:[1,1,0] op_sel_hi:[0,0,1]
	v_pk_add_f32 v[72:73], v[72:73], v[100:101]
	v_pk_fma_f32 v[76:77], v[100:101], v[24:25], v[76:77]
	v_pk_add_f32 v[74:75], v[74:75], v[102:103]
	v_pk_add_f32 v[72:73], v[72:73], v[102:103]
	v_pk_fma_f32 v[76:77], v[102:103], v[28:29], v[76:77]
	v_pk_fma_f32 v[78:79], v[102:103], v[26:27], v[78:79]
	v_sub_f32_e32 v96, v26, v9
	v_sub_f32_e32 v98, v28, v11
	v_sub_f32_e32 v100, v27, v12
	v_sub_f32_e32 v102, v29, v14
	v_sub_f32_e32 v97, v26, v17
	v_sub_f32_e32 v99, v25, v18
	v_sub_f32_e32 v101, v28, v19
	v_sub_f32_e32 v103, v27, v20
	v_fma_f32 v96, -v96, v96, s26
	v_fma_f32 v98, -v98, v98, s26
	v_fma_f32 v100, -v100, v100, s26
	v_fma_f32 v102, -v102, v102, s26
	v_fma_f32 v97, -v97, v97, s24
	v_fma_f32 v99, -v99, v99, s24
	v_fma_f32 v101, -v101, v101, s24
	v_fma_f32 v103, -v103, v103, s24
	v_exp_f32_e32 v96, v96
	v_exp_f32_e32 v98, v98
	v_exp_f32_e32 v100, v100
	v_exp_f32_e32 v102, v102
	v_exp_f32_e32 v97, v97
	v_exp_f32_e32 v99, v99
	v_exp_f32_e32 v101, v101
	v_exp_f32_e32 v103, v103
	v_pk_add_f32 v[74:75], v[74:75], v[104:105]
	v_pk_fma_f32 v[78:79], v[104:105], v[30:31], v[78:79]
	v_sub_f32_e32 v108, v30, v21
	v_sub_f32_e32 v110, v29, v22
	v_sub_f32_e32 v105, v26, v25
	v_sub_f32_e32 v104, v27, v26
	v_sub_f32_e32 v107, v28, v27
	v_sub_f32_e32 v106, v29, v28
	v_sub_f32_e32 v109, v30, v29
	s_nop 0
	v_fma_f32 v108, -v108, v108, s24
	v_fma_f32 v110, -v110, v110, s24
	v_fma_f32 v105, -v105, v105, s20
	v_fma_f32 v104, -v104, v104, s20
	v_fma_f32 v107, -v107, v107, s20
	v_fma_f32 v106, -v106, v106, s20
	v_fma_f32 v109, -v109, v109, s20
	v_exp_f32_e32 v108, v108
	v_exp_f32_e32 v110, v110
	v_exp_f32_e32 v105, v105
	v_exp_f32_e32 v104, v104
	v_exp_f32_e32 v107, v107
	v_exp_f32_e32 v106, v106
	v_exp_f32_e32 v109, v109
	v_add_f32_e32 v72, v72, v96
	v_fmac_f32_e32 v76, v96, v9
	v_add_f32_e32 v74, v74, v98
	v_fmac_f32_e32 v78, v98, v11
	v_add_f32_e32 v73, v73, v100
	v_fmac_f32_e32 v77, v100, v12
	v_add_f32_e32 v75, v75, v102
	v_fmac_f32_e32 v79, v102, v14
	v_add_f32_e32 v72, v72, v97
	v_fmac_f32_e32 v76, v97, v17
	v_add_f32_e32 v64, v64, v99
	v_fmac_f32_e32 v68, v99, v25
	v_add_f32_e32 v65, v65, v101
	v_fmac_f32_e32 v69, v101, v28
	v_add_f32_e32 v74, v74, v101
	v_fmac_f32_e32 v78, v101, v19
	v_add_f32_e32 v66, v66, v103
	v_fmac_f32_e32 v70, v103, v27
	v_add_f32_e32 v73, v73, v103
	v_fmac_f32_e32 v77, v103, v20
	v_add_f32_e32 v67, v67, v108
	v_fmac_f32_e32 v71, v108, v30
	v_add_f32_e32 v75, v75, v110
	v_fmac_f32_e32 v79, v110, v22
	v_add_f32_e32 v72, v72, v105
	v_fmac_f32_e32 v76, v105, v25
	v_add_f32_e32 v73, v73, v107
	v_fmac_f32_e32 v77, v107, v28
	v_add_f32_e32 v74, v74, v107
	v_fmac_f32_e32 v78, v107, v27
	v_add_f32_e32 v75, v75, v109
	v_fmac_f32_e32 v79, v109, v30
	s_nop 0
	v_pk_add_f32 v[72:73], v[72:73], v[104:105] op_sel_hi:[1,0]
	v_pk_fma_f32 v[76:77], v[104:105], v[26:27], v[76:77] op_sel:[0,1,0] op_sel_hi:[0,0,1]
	v_pk_add_f32 v[74:75], v[74:75], v[106:107] op_sel_hi:[1,0]
	v_pk_fma_f32 v[78:79], v[106:107], v[28:29], v[78:79] op_sel:[0,1,0] op_sel_hi:[0,0,1]
	s_waitcnt vmcnt(9)
	s_nop 0
	v_mov_b32_dpp v32, v36 row_shr:1 row_mask:0xf bank_mask:0xf
	v_mov_b32_dpp v33, v37 row_shr:1 row_mask:0xf bank_mask:0xf
	v_mov_b32_dpp v38, v34 row_shl:1 row_mask:0xf bank_mask:0xf
	v_mov_b32_dpp v39, v35 row_shl:1 row_mask:0xf bank_mask:0xf
	v_pk_mul_f32 v[34:35], v[34:35], s[32:33]
	v_pk_mul_f32 v[36:37], v[36:37], s[32:33]
	v_cndmask_b32_e64 v33, v33, v32, vcc
	v_cndmask_b32_e64 v38, v38, v39, s[16:17]
	v_pk_mul_f32 v[84:85], v[34:35], s[30:31]
	v_pk_mul_f32 v[86:87], v[36:37], s[30:31]
	v_pk_mul_f32 v[32:33], v[32:33], s[32:33]
	v_pk_mul_f32 v[38:39], v[38:39], s[32:33]
	v_mov_b32_e32 v80, s30
	v_mov_b32_e32 v81, s30
	v_mov_b32_e32 v82, s30
	v_mov_b32_e32 v83, s30
	s_setprio 2
	s_nop 0
	v_pk_add_f32 v[96:97], v[34:35], v[16:17] neg_lo:[0,1] neg_hi:[0,1]
	v_pk_add_f32 v[98:99], v[32:33], v[18:19] neg_lo:[0,1] neg_hi:[0,1]
	v_pk_add_f32 v[100:101], v[34:35], v[18:19] neg_lo:[0,1] neg_hi:[0,1]
	v_pk_add_f32 v[102:103], v[36:37], v[18:19] neg_lo:[0,1] neg_hi:[0,1]
	v_pk_fma_f32 v[96:97], v[96:97], v[96:97], s[28:29] neg_lo:[1,0,0] neg_hi:[1,0,0]
	v_pk_fma_f32 v[98:99], v[98:99], v[98:99], s[28:29] neg_lo:[1,0,0] neg_hi:[1,0,0]
	v_pk_fma_f32 v[100:101], v[100:101], v[100:101], s[22:23] neg_lo:[1,0,0] neg_hi:[1,0,0]
	v_pk_fma_f32 v[102:103], v[102:103], v[102:103], s[28:29] neg_lo:[1,0,0] neg_hi:[1,0,0]
	v_exp_f32_e32 v96, v96
	v_exp_f32_e32 v97, v97
	v_exp_f32_e32 v98, v98
	v_exp_f32_e32 v99, v99
	v_exp_f32_e32 v100, v100
	v_exp_f32_e32 v101, v101
	v_exp_f32_e32 v102, v102
	v_exp_f32_e32 v103, v103
	v_pk_add_f32 v[104:105], v[34:35], v[20:21] neg_lo:[0,1] neg_hi:[0,1]
	v_pk_add_f32 v[106:107], v[36:37], v[20:21] neg_lo:[0,1] neg_hi:[0,1]
	v_pk_add_f32 v[108:109], v[38:39], v[20:21] neg_lo:[0,1] neg_hi:[0,1]
	v_pk_add_f32 v[110:111], v[36:37], v[22:23] neg_lo:[0,1] neg_hi:[0,1]
	v_pk_fma_f32 v[104:105], v[104:105], v[104:105], s[28:29] neg_lo:[1,0,0] neg_hi:[1,0,0]
	v_pk_fma_f32 v[106:107], v[106:107], v[106:107], s[22:23] neg_lo:[1,0,0] neg_hi:[1,0,0]
	v_pk_fma_f32 v[108:109], v[108:109], v[108:109], s[28:29] neg_lo:[1,0,0] neg_hi:[1,0,0]
	v_pk_fma_f32 v[110:111], v[110:111], v[110:111], s[28:29] neg_lo:[1,0,0] neg_hi:[1,0,0]
	v_exp_f32_e32 v104, v104
	v_exp_f32_e32 v105, v105
	v_exp_f32_e32 v106, v106
	v_exp_f32_e32 v107, v107
	v_exp_f32_e32 v108, v108
	v_exp_f32_e32 v109, v109
	v_exp_f32_e32 v110, v110
	v_exp_f32_e32 v111, v111
	v_pk_add_f32 v[80:81], v[80:81], v[96:97]
	v_pk_fma_f32 v[84:85], v[96:97], v[16:17], v[84:85]
	v_pk_add_f32 v[64:65], v[64:65], v[98:99]
	v_pk_fma_f32 v[68:69], v[98:99], v[32:33], v[68:69]
	v_pk_add_f32 v[80:81], v[80:81], v[100:101]
	v_pk_add_f32 v[64:65], v[64:65], v[100:101]
	v_pk_fma_f32 v[68:69], v[100:101], v[34:35], v[68:69]
	v_pk_fma_f32 v[84:85], v[100:101], v[18:19], v[84:85]
	v_pk_add_f32 v[64:65], v[64:65], v[102:103]
	v_pk_fma_f32 v[68:69], v[102:103], v[36:37], v[68:69]
	v_pk_add_f32 v[82:83], v[82:83], v[102:103]
	v_pk_fma_f32 v[86:87], v[102:103], v[18:19], v[86:87]
	v_pk_add_f32 v[96:97], v[34:35], v[18:19] op_sel:[1,0] op_sel_hi:[0,1] neg_lo:[0,1] neg_hi:[0,1]
	v_pk_add_f32 v[98:99], v[36:37], v[20:21] op_sel:[1,0] op_sel_hi:[0,1] neg_lo:[0,1] neg_hi:[0,1]
	v_pk_add_f32 v[100:101], v[34:35], v[24:25] neg_lo:[0,1] neg_hi:[0,1]
	v_pk_add_f32 v[102:103], v[32:33], v[26:27] neg_lo:[0,1] neg_hi:[0,1]
	v_pk_fma_f32 v[96:97], v[96:97], v[96:97], s[26:27] neg_lo:[1,0,0] neg_hi:[1,0,0]
	v_pk_fma_f32 v[98:99], v[98:99], v[98:99], s[26:27] neg_lo:[1,0,0] neg_hi:[1,0,0]
	v_pk_fma_f32 v[100:101], v[100:101], v[100:101], s[26:27] neg_lo:[1,0,0] neg_hi:[1,0,0]
	v_pk_fma_f32 v[102:103], v[102:103], v[102:103], s[26:27] neg_lo:[1,0,0] neg_hi:[1,0,0]
	v_exp_f32_e32 v96, v96
	v_exp_f32_e32 v97, v97
	v_exp_f32_e32 v98, v98
	v_exp_f32_e32 v99, v99
	v_exp_f32_e32 v100, v100
	v_exp_f32_e32 v101, v101
	v_exp_f32_e32 v102, v102
	v_exp_f32_e32 v103, v103
	v_pk_add_f32 v[66:67], v[66:67], v[104:105]
	v_pk_fma_f32 v[70:71], v[104:105], v[34:35], v[70:71]
	v_pk_add_f32 v[80:81], v[80:81], v[104:105]
	v_pk_fma_f32 v[84:85], v[104:105], v[20:21], v[84:85]
	v_pk_add_f32 v[66:67], v[66:67], v[106:107]
	v_pk_fma_f32 v[70:71], v[106:107], v[36:37], v[70:71]
	v_pk_add_f32 v[82:83], v[82:83], v[106:107]
	v_pk_fma_f32 v[86:87], v[106:107], v[20:21], v[86:87]
	v_pk_add_f32 v[66:67], v[66:67], v[108:109]
	v_pk_fma_f32 v[70:71], v[108:109], v[38:39], v[70:71]
	v_pk_add_f32 v[82:83], v[82:83], v[110:111]
	v_pk_fma_f32 v[86:87], v[110:111], v[22:23], v[86:87]
	v_pk_add_f32 v[104:105], v[34:35], v[26:27] neg_lo:[0,1] neg_hi:[0,1]
	v_pk_add_f32 v[106:107], v[36:37], v[26:27] neg_lo:[0,1] neg_hi:[0,1]
	v_pk_add_f32 v[108:109], v[34:35], v[28:29] neg_lo:[0,1] neg_hi:[0,1]
	v_pk_add_f32 v[110:111], v[36:37], v[28:29] neg_lo:[0,1] neg_hi:[0,1]
	v_pk_fma_f32 v[104:105], v[104:105], v[104:105], s[20:21] neg_lo:[1,0,0] neg_hi:[1,0,0]
	v_pk_fma_f32 v[106:107], v[106:107], v[106:107], s[26:27] neg_lo:[1,0,0] neg_hi:[1,0,0]
	v_pk_fma_f32 v[108:109], v[108:109], v[108:109], s[26:27] neg_lo:[1,0,0] neg_hi:[1,0,0]
	v_pk_fma_f32 v[110:111], v[110:111], v[110:111], s[20:21] neg_lo:[1,0,0] neg_hi:[1,0,0]
	v_exp_f32_e32 v104, v104
	v_exp_f32_e32 v105, v105
	v_exp_f32_e32 v106, v106
	v_exp_f32_e32 v107, v107
	v_exp_f32_e32 v108, v108
	v_exp_f32_e32 v109, v109
	v_exp_f32_e32 v110, v110
	v_exp_f32_e32 v111, v111
	v_pk_add_f32 v[64:65], v[64:65], v[96:97]
	v_pk_fma_f32 v[68:69], v[96:97], v[34:35], v[68:69] op_sel:[0,1,0] op_sel_hi:[1,0,1]
	v_pk_add_f32 v[80:81], v[80:81], v[96:97] op_sel:[0,1] op_sel_hi:[1,0]
	v_pk_fma_f32 v[84:85], v[96:97], v[18:19], v[84:85] op_sel:[1,1,0] op_sel_hi:[0,0,1]
	v_pk_add_f32 v[66:67], v[66:67], v[98:99]
	v_pk_fma_f32 v[70:71], v[98:99], v[36:37], v[70:71] op_sel:[0,1,0] op_sel_hi:[1,0,1]
	v_pk_add_f32 v[82:83], v[82:83], v[98:99] op_sel:[0,1] op_sel_hi:[1,0]
	v_pk_fma_f32 v[86:87], v[98:99], v[20:21], v[86:87] op_sel:[1,1,0] op_sel_hi:[0,0,1]
	v_pk_add_f32 v[80:81], v[80:81], v[100:101]
	v_pk_fma_f32 v[84:85], v[100:101], v[24:25], v[84:85]
	v_pk_add_f32 v[72:73], v[72:73], v[102:103]
	v_pk_fma_f32 v[76:77], v[102:103], v[32:33], v[76:77]
	v_pk_add_f32 v[96:97], v[38:39], v[28:29] neg_lo:[0,1] neg_hi:[0,1]
	v_pk_add_f32 v[98:99], v[36:37], v[30:31] neg_lo:[0,1] neg_hi:[0,1]
	v_pk_add_f32 v[100:101], v[34:35], v[26:27] op_sel:[1,0] op_sel_hi:[0,1] neg_lo:[0,1] neg_hi:[0,1]
	v_pk_add_f32 v[102:103], v[36:37], v[28:29] op_sel:[1,0] op_sel_hi:[0,1] neg_lo:[0,1] neg_hi:[0,1]
	v_pk_fma_f32 v[96:97], v[96:97], v[96:97], s[26:27] neg_lo:[1,0,0] neg_hi:[1,0,0]
	v_pk_fma_f32 v[98:99], v[98:99], v[98:99], s[26:27] neg_lo:[1,0,0] neg_hi:[1,0,0]
	v_pk_fma_f32 v[100:101], v[100:101], v[100:101], s[24:25] neg_lo:[1,0,0] neg_hi:[1,0,0]
	v_pk_fma_f32 v[102:103], v[102:103], v[102:103], s[24:25] neg_lo:[1,0,0] neg_hi:[1,0,0]
	v_exp_f32_e32 v96, v96
	v_exp_f32_e32 v97, v97
	v_exp_f32_e32 v98, v98
	v_exp_f32_e32 v99, v99
	v_exp_f32_e32 v100, v100
	v_exp_f32_e32 v101, v101
	v_exp_f32_e32 v102, v102
	v_exp_f32_e32 v103, v103
	v_pk_add_f32 v[72:73], v[72:73], v[104:105]
	v_pk_fma_f32 v[76:77], v[104:105], v[34:35], v[76:77]
	v_pk_add_f32 v[80:81], v[80:81], v[104:105]
	v_pk_fma_f32 v[84:85], v[104:105], v[26:27], v[84:85]
	v_pk_add_f32 v[72:73], v[72:73], v[106:107]
	v_pk_fma_f32 v[76:77], v[106:107], v[36:37], v[76:77]
	v_pk_add_f32 v[82:83], v[82:83], v[106:107]
	v_pk_fma_f32 v[86:87], v[106:107], v[26:27], v[86:87]
	v_pk_add_f32 v[74:75], v[74:75], v[108:109]
	v_pk_fma_f32 v[78:79], v[108:109], v[34:35], v[78:79]
	v_pk_add_f32 v[80:81], v[80:81], v[108:109]
	v_pk_fma_f32 v[84:85], v[108:109], v[28:29], v[84:85]
	v_pk_add_f32 v[74:75], v[74:75], v[110:111]
	v_pk_fma_f32 v[78:79], v[110:111], v[36:37], v[78:79]
	v_pk_add_f32 v[82:83], v[82:83], v[110:111]
	v_pk_fma_f32 v[86:87], v[110:111], v[28:29], v[86:87]
	v_pk_add_f32 v[104:105], v[34:35], v[32:33] neg_lo:[0,1] neg_hi:[0,1]
	v_pk_add_f32 v[106:107], v[36:37], v[34:35] neg_lo:[0,1] neg_hi:[0,1]
	v_pk_add_f32 v[108:109], v[38:39], v[36:37] neg_lo:[0,1] neg_hi:[0,1]
	v_pk_fma_f32 v[104:105], v[104:105], v[104:105], s[22:23] neg_lo:[1,0,0] neg_hi:[1,0,0]
	v_pk_fma_f32 v[106:107], v[106:107], v[106:107], s[22:23] neg_lo:[1,0,0] neg_hi:[1,0,0]
	v_pk_fma_f32 v[108:109], v[108:109], v[108:109], s[22:23] neg_lo:[1,0,0] neg_hi:[1,0,0]
	v_exp_f32_e32 v104, v104
	v_exp_f32_e32 v105, v105
	v_exp_f32_e32 v106, v106
	v_exp_f32_e32 v107, v107
	v_exp_f32_e32 v108, v108
	v_exp_f32_e32 v109, v109
	v_pk_add_f32 v[74:75], v[74:75], v[96:97]
	v_pk_fma_f32 v[78:79], v[96:97], v[38:39], v[78:79]
	v_pk_add_f32 v[82:83], v[82:83], v[98:99]
	v_pk_fma_f32 v[86:87], v[98:99], v[30:31], v[86:87]
	v_pk_add_f32 v[72:73], v[72:73], v[100:101]
	v_pk_fma_f32 v[76:77], v[100:101], v[34:35], v[76:77] op_sel:[0,1,0] op_sel_hi:[1,0,1]
	v_pk_add_f32 v[80:81], v[80:81], v[100:101] op_sel:[0,1] op_sel_hi:[1,0]
	v_pk_fma_f32 v[84:85], v[100:101], v[26:27], v[84:85] op_sel:[1,1,0] op_sel_hi:[0,0,1]
	v_pk_add_f32 v[74:75], v[74:75], v[102:103]
	v_pk_fma_f32 v[78:79], v[102:103], v[36:37], v[78:79] op_sel:[0,1,0] op_sel_hi:[1,0,1]
	v_pk_add_f32 v[82:83], v[82:83], v[102:103] op_sel:[0,1] op_sel_hi:[1,0]
	v_pk_fma_f32 v[86:87], v[102:103], v[28:29], v[86:87] op_sel:[1,1,0] op_sel_hi:[0,0,1]
	v_sub_f32_e32 v96, v34, v17
	v_sub_f32_e32 v98, v33, v18
	v_sub_f32_e32 v100, v36, v19
	v_sub_f32_e32 v102, v35, v20
	v_sub_f32_e32 v97, v38, v21
	v_sub_f32_e32 v99, v37, v22
	v_sub_f32_e32 v101, v34, v25
	v_sub_f32_e32 v103, v33, v26
	v_fma_f32 v96, -v96, v96, s26
	v_fma_f32 v98, -v98, v98, s26
	v_fma_f32 v100, -v100, v100, s26
	v_fma_f32 v102, -v102, v102, s26
	v_fma_f32 v97, -v97, v97, s26
	v_fma_f32 v99, -v99, v99, s26
	v_fma_f32 v101, -v101, v101, s24
	v_fma_f32 v103, -v103, v103, s24
	v_exp_f32_e32 v96, v96
	v_exp_f32_e32 v98, v98
	v_exp_f32_e32 v100, v100
	v_exp_f32_e32 v102, v102
	v_exp_f32_e32 v97, v97
	v_exp_f32_e32 v99, v99
	v_exp_f32_e32 v101, v101
	v_exp_f32_e32 v103, v103
	v_pk_add_f32 v[80:81], v[80:81], v[104:105]
	v_pk_fma_f32 v[84:85], v[104:105], v[32:33], v[84:85]
	v_pk_add_f32 v[82:83], v[82:83], v[106:107]
	v_pk_add_f32 v[80:81], v[80:81], v[106:107]
	v_pk_fma_f32 v[84:85], v[106:107], v[36:37], v[84:85]
	v_pk_fma_f32 v[86:87], v[106:107], v[34:35], v[86:87]
	v_pk_add_f32 v[82:83], v[82:83], v[108:109]
	v_pk_fma_f32 v[86:87], v[108:109], v[38:39], v[86:87]
	v_sub_f32_e32 v108, v36, v27
	v_sub_f32_e32 v110, v35, v28
	v_sub_f32_e32 v105, v38, v29
	v_sub_f32_e32 v107, v37, v30
	v_sub_f32_e32 v109, v34, v33
	v_sub_f32_e32 v104, v35, v34
	v_sub_f32_e32 v111, v36, v35
	v_sub_f32_e32 v106, v37, v36
	v_fma_f32 v108, -v108, v108, s24
	v_fma_f32 v110, -v110, v110, s24
	v_fma_f32 v105, -v105, v105, s24
	v_fma_f32 v107, -v107, v107, s24
	v_fma_f32 v109, -v109, v109, s20
	v_fma_f32 v104, -v104, v104, s20
	v_fma_f32 v111, -v111, v111, s20
	v_fma_f32 v106, -v106, v106, s20
	v_exp_f32_e32 v108, v108
	v_exp_f32_e32 v110, v110
	v_exp_f32_e32 v105, v105
	v_exp_f32_e32 v107, v107
	v_exp_f32_e32 v109, v109
	v_exp_f32_e32 v104, v104
	v_exp_f32_e32 v111, v111
	v_exp_f32_e32 v106, v106
	v_add_f32_e32 v80, v80, v96
	v_fmac_f32_e32 v84, v96, v17
	v_add_f32_e32 v64, v64, v98
	v_fmac_f32_e32 v68, v98, v33
	v_add_f32_e32 v65, v65, v100
	v_fmac_f32_e32 v69, v100, v36
	v_add_f32_e32 v82, v82, v100
	v_fmac_f32_e32 v86, v100, v19
	v_add_f32_e32 v66, v66, v102
	v_fmac_f32_e32 v70, v102, v35
	v_add_f32_e32 v81, v81, v102
	v_fmac_f32_e32 v85, v102, v20
	v_add_f32_e32 v67, v67, v97
	v_fmac_f32_e32 v71, v97, v38
	v_add_f32_e32 v83, v83, v99
	v_fmac_f32_e32 v87, v99, v22
	v_add_f32_e32 v80, v80, v101
	v_fmac_f32_e32 v84, v101, v25
	v_add_f32_e32 v72, v72, v103
	v_fmac_f32_e32 v76, v103, v33
	v_sub_f32_e32 v96, v38, v37
	s_nop 0
	v_fma_f32 v96, -v96, v96, s20
	s_nop 0
	v_exp_f32_e32 v96, v96
	s_nop 0
	v_add_f32_e32 v73, v73, v108
	v_fmac_f32_e32 v77, v108, v36
	v_add_f32_e32 v82, v82, v108
	v_fmac_f32_e32 v86, v108, v27
	v_add_f32_e32 v74, v74, v110
	v_fmac_f32_e32 v78, v110, v35
	v_add_f32_e32 v81, v81, v110
	v_fmac_f32_e32 v85, v110, v28
	v_add_f32_e32 v75, v75, v105
	v_fmac_f32_e32 v79, v105, v38
	v_add_f32_e32 v83, v83, v107
	v_fmac_f32_e32 v87, v107, v30
	v_add_f32_e32 v80, v80, v109
	v_fmac_f32_e32 v84, v109, v33
	v_add_f32_e32 v81, v81, v111
	v_fmac_f32_e32 v85, v111, v36
	v_add_f32_e32 v82, v82, v111
	v_fmac_f32_e32 v86, v111, v35
	s_nop 0
	v_pk_add_f32 v[80:81], v[80:81], v[104:105] op_sel_hi:[1,0]
	v_pk_fma_f32 v[84:85], v[104:105], v[34:35], v[84:85] op_sel:[0,1,0] op_sel_hi:[0,0,1]
	v_pk_add_f32 v[82:83], v[82:83], v[106:107] op_sel_hi:[1,0]
	v_pk_fma_f32 v[86:87], v[106:107], v[36:37], v[86:87] op_sel:[0,1,0] op_sel_hi:[0,0,1]
	v_add_f32_e32 v83, v83, v96
	v_fmac_f32_e32 v87, v96, v38
	v_rcp_f32_e32 v96, v64
	v_rcp_f32_e32 v97, v65
	v_rcp_f32_e32 v98, v66
	v_rcp_f32_e32 v99, v67
	v_pk_mul_f32 v[68:69], v[68:69], s[34:35]
	v_pk_mul_f32 v[70:71], v[70:71], s[34:35]
	v_pk_mul_f32 v[68:69], v[68:69], v[96:97]
	v_pk_mul_f32 v[70:71], v[70:71], v[98:99]
	s_nop 0
	s_nop 0
	buffer_store_dwordx4 v[68:71], v114, s[12:15], 0 offen sc1
	s_waitcnt vmcnt(7)
	s_nop 0
	v_mov_b32_dpp v40, v44 row_shr:1 row_mask:0xf bank_mask:0xf
	v_mov_b32_dpp v41, v45 row_shr:1 row_mask:0xf bank_mask:0xf
	v_mov_b32_dpp v46, v42 row_shl:1 row_mask:0xf bank_mask:0xf
	v_mov_b32_dpp v47, v43 row_shl:1 row_mask:0xf bank_mask:0xf
	v_pk_mul_f32 v[42:43], v[42:43], s[32:33]
	v_pk_mul_f32 v[44:45], v[44:45], s[32:33]
	v_cndmask_b32_e64 v41, v41, v40, vcc
	v_cndmask_b32_e64 v46, v46, v47, s[16:17]
	v_pk_mul_f32 v[92:93], v[42:43], s[30:31]
	v_pk_mul_f32 v[94:95], v[44:45], s[30:31]
	v_pk_mul_f32 v[40:41], v[40:41], s[32:33]
	v_pk_mul_f32 v[46:47], v[46:47], s[32:33]
	v_mov_b32_e32 v88, s30
	v_mov_b32_e32 v89, s30
	v_mov_b32_e32 v90, s30
	v_mov_b32_e32 v91, s30
	s_setprio 1
	s_nop 0
	v_pk_add_f32 v[96:97], v[42:43], v[24:25] neg_lo:[0,1] neg_hi:[0,1]
	v_pk_add_f32 v[98:99], v[40:41], v[26:27] neg_lo:[0,1] neg_hi:[0,1]
	v_pk_add_f32 v[100:101], v[42:43], v[26:27] neg_lo:[0,1] neg_hi:[0,1]
	v_pk_add_f32 v[102:103], v[44:45], v[26:27] neg_lo:[0,1] neg_hi:[0,1]
	v_pk_fma_f32 v[96:97], v[96:97], v[96:97], s[28:29] neg_lo:[1,0,0] neg_hi:[1,0,0]
	v_pk_fma_f32 v[98:99], v[98:99], v[98:99], s[28:29] neg_lo:[1,0,0] neg_hi:[1,0,0]
	v_pk_fma_f32 v[100:101], v[100:101], v[100:101], s[22:23] neg_lo:[1,0,0] neg_hi:[1,0,0]
	v_pk_fma_f32 v[102:103], v[102:103], v[102:103], s[28:29] neg_lo:[1,0,0] neg_hi:[1,0,0]
	v_exp_f32_e32 v96, v96
	v_exp_f32_e32 v97, v97
	v_exp_f32_e32 v98, v98
	v_exp_f32_e32 v99, v99
	v_exp_f32_e32 v100, v100
	v_exp_f32_e32 v101, v101
	v_exp_f32_e32 v102, v102
	v_exp_f32_e32 v103, v103
	v_pk_add_f32 v[104:105], v[42:43], v[28:29] neg_lo:[0,1] neg_hi:[0,1]
	v_pk_add_f32 v[106:107], v[44:45], v[28:29] neg_lo:[0,1] neg_hi:[0,1]
	v_pk_add_f32 v[108:109], v[46:47], v[28:29] neg_lo:[0,1] neg_hi:[0,1]
	v_pk_add_f32 v[110:111], v[44:45], v[30:31] neg_lo:[0,1] neg_hi:[0,1]
	v_pk_fma_f32 v[104:105], v[104:105], v[104:105], s[28:29] neg_lo:[1,0,0] neg_hi:[1,0,0]
	v_pk_fma_f32 v[106:107], v[106:107], v[106:107], s[22:23] neg_lo:[1,0,0] neg_hi:[1,0,0]
	v_pk_fma_f32 v[108:109], v[108:109], v[108:109], s[28:29] neg_lo:[1,0,0] neg_hi:[1,0,0]
	v_pk_fma_f32 v[110:111], v[110:111], v[110:111], s[28:29] neg_lo:[1,0,0] neg_hi:[1,0,0]
	v_exp_f32_e32 v104, v104
	v_exp_f32_e32 v105, v105
	v_exp_f32_e32 v106, v106
	v_exp_f32_e32 v107, v107
	v_exp_f32_e32 v108, v108
	v_exp_f32_e32 v109, v109
	v_exp_f32_e32 v110, v110
	v_exp_f32_e32 v111, v111
	v_pk_add_f32 v[88:89], v[88:89], v[96:97]
	v_pk_fma_f32 v[92:93], v[96:97], v[24:25], v[92:93]
	v_pk_add_f32 v[72:73], v[72:73], v[98:99]
	v_pk_fma_f32 v[76:77], v[98:99], v[40:41], v[76:77]
	v_pk_add_f32 v[88:89], v[88:89], v[100:101]
	v_pk_add_f32 v[72:73], v[72:73], v[100:101]
	v_pk_fma_f32 v[76:77], v[100:101], v[42:43], v[76:77]
	v_pk_fma_f32 v[92:93], v[100:101], v[26:27], v[92:93]
	v_pk_add_f32 v[72:73], v[72:73], v[102:103]
	v_pk_fma_f32 v[76:77], v[102:103], v[44:45], v[76:77]
	v_pk_add_f32 v[90:91], v[90:91], v[102:103]
	v_pk_fma_f32 v[94:95], v[102:103], v[26:27], v[94:95]
	v_pk_add_f32 v[96:97], v[42:43], v[26:27] op_sel:[1,0] op_sel_hi:[0,1] neg_lo:[0,1] neg_hi:[0,1]
	v_pk_add_f32 v[98:99], v[44:45], v[28:29] op_sel:[1,0] op_sel_hi:[0,1] neg_lo:[0,1] neg_hi:[0,1]
	v_pk_add_f32 v[100:101], v[42:43], v[32:33] neg_lo:[0,1] neg_hi:[0,1]
	v_pk_add_f32 v[102:103], v[40:41], v[34:35] neg_lo:[0,1] neg_hi:[0,1]
	v_pk_fma_f32 v[96:97], v[96:97], v[96:97], s[26:27] neg_lo:[1,0,0] neg_hi:[1,0,0]
	v_pk_fma_f32 v[98:99], v[98:99], v[98:99], s[26:27] neg_lo:[1,0,0] neg_hi:[1,0,0]
	v_pk_fma_f32 v[100:101], v[100:101], v[100:101], s[26:27] neg_lo:[1,0,0] neg_hi:[1,0,0]
	v_pk_fma_f32 v[102:103], v[102:103], v[102:103], s[26:27] neg_lo:[1,0,0] neg_hi:[1,0,0]
	v_exp_f32_e32 v96, v96
	v_exp_f32_e32 v97, v97
	v_exp_f32_e32 v98, v98
	v_exp_f32_e32 v99, v99
	v_exp_f32_e32 v100, v100
	v_exp_f32_e32 v101, v101
	v_exp_f32_e32 v102, v102
	v_exp_f32_e32 v103, v103
	v_pk_add_f32 v[74:75], v[74:75], v[104:105]
	v_pk_fma_f32 v[78:79], v[104:105], v[42:43], v[78:79]
	v_pk_add_f32 v[88:89], v[88:89], v[104:105]
	v_pk_fma_f32 v[92:93], v[104:105], v[28:29], v[92:93]
	v_pk_add_f32 v[74:75], v[74:75], v[106:107]
	v_pk_fma_f32 v[78:79], v[106:107], v[44:45], v[78:79]
	v_pk_add_f32 v[90:91], v[90:91], v[106:107]
	v_pk_fma_f32 v[94:95], v[106:107], v[28:29], v[94:95]
	v_pk_add_f32 v[74:75], v[74:75], v[108:109]
	v_pk_fma_f32 v[78:79], v[108:109], v[46:47], v[78:79]
	v_pk_add_f32 v[90:91], v[90:91], v[110:111]
	v_pk_fma_f32 v[94:95], v[110:111], v[30:31], v[94:95]
	v_pk_add_f32 v[104:105], v[42:43], v[34:35] neg_lo:[0,1] neg_hi:[0,1]
	v_pk_add_f32 v[106:107], v[44:45], v[34:35] neg_lo:[0,1] neg_hi:[0,1]
	v_pk_add_f32 v[108:109], v[42:43], v[36:37] neg_lo:[0,1] neg_hi:[0,1]
	v_pk_add_f32 v[110:111], v[44:45], v[36:37] neg_lo:[0,1] neg_hi:[0,1]
	v_pk_fma_f32 v[104:105], v[104:105], v[104:105], s[20:21] neg_lo:[1,0,0] neg_hi:[1,0,0]
	v_pk_fma_f32 v[106:107], v[106:107], v[106:107], s[26:27] neg_lo:[1,0,0] neg_hi:[1,0,0]
	v_pk_fma_f32 v[108:109], v[108:109], v[108:109], s[26:27] neg_lo:[1,0,0] neg_hi:[1,0,0]
	v_pk_fma_f32 v[110:111], v[110:111], v[110:111], s[20:21] neg_lo:[1,0,0] neg_hi:[1,0,0]
	v_exp_f32_e32 v104, v104
	v_exp_f32_e32 v105, v105
	v_exp_f32_e32 v106, v106
	v_exp_f32_e32 v107, v107
	v_exp_f32_e32 v108, v108
	v_exp_f32_e32 v109, v109
	v_exp_f32_e32 v110, v110
	v_exp_f32_e32 v111, v111
	v_pk_add_f32 v[72:73], v[72:73], v[96:97]
	v_pk_fma_f32 v[76:77], v[96:97], v[42:43], v[76:77] op_sel:[0,1,0] op_sel_hi:[1,0,1]
	v_pk_add_f32 v[88:89], v[88:89], v[96:97] op_sel:[0,1] op_sel_hi:[1,0]
	v_pk_fma_f32 v[92:93], v[96:97], v[26:27], v[92:93] op_sel:[1,1,0] op_sel_hi:[0,0,1]
	v_pk_add_f32 v[74:75], v[74:75], v[98:99]
	v_pk_fma_f32 v[78:79], v[98:99], v[44:45], v[78:79] op_sel:[0,1,0] op_sel_hi:[1,0,1]
	v_pk_add_f32 v[90:91], v[90:91], v[98:99] op_sel:[0,1] op_sel_hi:[1,0]
	v_pk_fma_f32 v[94:95], v[98:99], v[28:29], v[94:95] op_sel:[1,1,0] op_sel_hi:[0,0,1]
	v_pk_add_f32 v[88:89], v[88:89], v[100:101]
	v_pk_fma_f32 v[92:93], v[100:101], v[32:33], v[92:93]
	v_pk_add_f32 v[80:81], v[80:81], v[102:103]
	v_pk_fma_f32 v[84:85], v[102:103], v[40:41], v[84:85]
	v_pk_add_f32 v[96:97], v[46:47], v[36:37] neg_lo:[0,1] neg_hi:[0,1]
	v_pk_add_f32 v[98:99], v[44:45], v[38:39] neg_lo:[0,1] neg_hi:[0,1]
	v_pk_add_f32 v[100:101], v[42:43], v[34:35] op_sel:[1,0] op_sel_hi:[0,1] neg_lo:[0,1] neg_hi:[0,1]
	v_pk_add_f32 v[102:103], v[44:45], v[36:37] op_sel:[1,0] op_sel_hi:[0,1] neg_lo:[0,1] neg_hi:[0,1]
	v_pk_fma_f32 v[96:97], v[96:97], v[96:97], s[26:27] neg_lo:[1,0,0] neg_hi:[1,0,0]
	v_pk_fma_f32 v[98:99], v[98:99], v[98:99], s[26:27] neg_lo:[1,0,0] neg_hi:[1,0,0]
	v_pk_fma_f32 v[100:101], v[100:101], v[100:101], s[24:25] neg_lo:[1,0,0] neg_hi:[1,0,0]
	v_pk_fma_f32 v[102:103], v[102:103], v[102:103], s[24:25] neg_lo:[1,0,0] neg_hi:[1,0,0]
	v_exp_f32_e32 v96, v96
	v_exp_f32_e32 v97, v97
	v_exp_f32_e32 v98, v98
	v_exp_f32_e32 v99, v99
	v_exp_f32_e32 v100, v100
	v_exp_f32_e32 v101, v101
	v_exp_f32_e32 v102, v102
	v_exp_f32_e32 v103, v103
	v_pk_add_f32 v[80:81], v[80:81], v[104:105]
	v_pk_fma_f32 v[84:85], v[104:105], v[42:43], v[84:85]
	v_pk_add_f32 v[88:89], v[88:89], v[104:105]
	v_pk_fma_f32 v[92:93], v[104:105], v[34:35], v[92:93]
	v_pk_add_f32 v[80:81], v[80:81], v[106:107]
	v_pk_fma_f32 v[84:85], v[106:107], v[44:45], v[84:85]
	v_pk_add_f32 v[90:91], v[90:91], v[106:107]
	v_pk_fma_f32 v[94:95], v[106:107], v[34:35], v[94:95]
	v_pk_add_f32 v[82:83], v[82:83], v[108:109]
	v_pk_fma_f32 v[86:87], v[108:109], v[42:43], v[86:87]
	v_pk_add_f32 v[88:89], v[88:89], v[108:109]
	v_pk_fma_f32 v[92:93], v[108:109], v[36:37], v[92:93]
	v_pk_add_f32 v[82:83], v[82:83], v[110:111]
	v_pk_fma_f32 v[86:87], v[110:111], v[44:45], v[86:87]
	v_pk_add_f32 v[90:91], v[90:91], v[110:111]
	v_pk_fma_f32 v[94:95], v[110:111], v[36:37], v[94:95]
	v_pk_add_f32 v[104:105], v[42:43], v[40:41] neg_lo:[0,1] neg_hi:[0,1]
	v_pk_add_f32 v[106:107], v[44:45], v[42:43] neg_lo:[0,1] neg_hi:[0,1]
	v_pk_add_f32 v[108:109], v[46:47], v[44:45] neg_lo:[0,1] neg_hi:[0,1]
	v_pk_fma_f32 v[104:105], v[104:105], v[104:105], s[22:23] neg_lo:[1,0,0] neg_hi:[1,0,0]
	v_pk_fma_f32 v[106:107], v[106:107], v[106:107], s[22:23] neg_lo:[1,0,0] neg_hi:[1,0,0]
	v_pk_fma_f32 v[108:109], v[108:109], v[108:109], s[22:23] neg_lo:[1,0,0] neg_hi:[1,0,0]
	v_exp_f32_e32 v104, v104
	v_exp_f32_e32 v105, v105
	v_exp_f32_e32 v106, v106
	v_exp_f32_e32 v107, v107
	v_exp_f32_e32 v108, v108
	v_exp_f32_e32 v109, v109
	v_pk_add_f32 v[82:83], v[82:83], v[96:97]
	v_pk_fma_f32 v[86:87], v[96:97], v[46:47], v[86:87]
	v_pk_add_f32 v[90:91], v[90:91], v[98:99]
	v_pk_fma_f32 v[94:95], v[98:99], v[38:39], v[94:95]
	v_pk_add_f32 v[80:81], v[80:81], v[100:101]
	v_pk_fma_f32 v[84:85], v[100:101], v[42:43], v[84:85] op_sel:[0,1,0] op_sel_hi:[1,0,1]
	v_pk_add_f32 v[88:89], v[88:89], v[100:101] op_sel:[0,1] op_sel_hi:[1,0]
	v_pk_fma_f32 v[92:93], v[100:101], v[34:35], v[92:93] op_sel:[1,1,0] op_sel_hi:[0,0,1]
	v_pk_add_f32 v[82:83], v[82:83], v[102:103]
	v_pk_fma_f32 v[86:87], v[102:103], v[44:45], v[86:87] op_sel:[0,1,0] op_sel_hi:[1,0,1]
	v_pk_add_f32 v[90:91], v[90:91], v[102:103] op_sel:[0,1] op_sel_hi:[1,0]
	v_pk_fma_f32 v[94:95], v[102:103], v[36:37], v[94:95] op_sel:[1,1,0] op_sel_hi:[0,0,1]
	v_sub_f32_e32 v96, v42, v25
	v_sub_f32_e32 v98, v41, v26
	v_sub_f32_e32 v100, v44, v27
	v_sub_f32_e32 v102, v43, v28
	v_sub_f32_e32 v97, v46, v29
	v_sub_f32_e32 v99, v45, v30
	v_sub_f32_e32 v101, v42, v33
	v_sub_f32_e32 v103, v41, v34
	v_fma_f32 v96, -v96, v96, s26
	v_fma_f32 v98, -v98, v98, s26
	v_fma_f32 v100, -v100, v100, s26
	v_fma_f32 v102, -v102, v102, s26
	v_fma_f32 v97, -v97, v97, s26
	v_fma_f32 v99, -v99, v99, s26
	v_fma_f32 v101, -v101, v101, s24
	v_fma_f32 v103, -v103, v103, s24
	v_exp_f32_e32 v96, v96
	v_exp_f32_e32 v98, v98
	v_exp_f32_e32 v100, v100
	v_exp_f32_e32 v102, v102
	v_exp_f32_e32 v97, v97
	v_exp_f32_e32 v99, v99
	v_exp_f32_e32 v101, v101
	v_exp_f32_e32 v103, v103
	v_pk_add_f32 v[88:89], v[88:89], v[104:105]
	v_pk_fma_f32 v[92:93], v[104:105], v[40:41], v[92:93]
	v_pk_add_f32 v[90:91], v[90:91], v[106:107]
	v_pk_add_f32 v[88:89], v[88:89], v[106:107]
	v_pk_fma_f32 v[92:93], v[106:107], v[44:45], v[92:93]
	v_pk_fma_f32 v[94:95], v[106:107], v[42:43], v[94:95]
	v_pk_add_f32 v[90:91], v[90:91], v[108:109]
	v_pk_fma_f32 v[94:95], v[108:109], v[46:47], v[94:95]
	v_sub_f32_e32 v108, v44, v35
	v_sub_f32_e32 v110, v43, v36
	v_sub_f32_e32 v105, v46, v37
	v_sub_f32_e32 v107, v45, v38
	v_sub_f32_e32 v109, v42, v41
	v_sub_f32_e32 v104, v43, v42
	v_sub_f32_e32 v111, v44, v43
	v_sub_f32_e32 v106, v45, v44
	v_fma_f32 v108, -v108, v108, s24
	v_fma_f32 v110, -v110, v110, s24
	v_fma_f32 v105, -v105, v105, s24
	v_fma_f32 v107, -v107, v107, s24
	v_fma_f32 v109, -v109, v109, s20
	v_fma_f32 v104, -v104, v104, s20
	v_fma_f32 v111, -v111, v111, s20
	v_fma_f32 v106, -v106, v106, s20
	v_exp_f32_e32 v108, v108
	v_exp_f32_e32 v110, v110
	v_exp_f32_e32 v105, v105
	v_exp_f32_e32 v107, v107
	v_exp_f32_e32 v109, v109
	v_exp_f32_e32 v104, v104
	v_exp_f32_e32 v111, v111
	v_exp_f32_e32 v106, v106
	v_add_f32_e32 v88, v88, v96
	v_fmac_f32_e32 v92, v96, v25
	v_add_f32_e32 v72, v72, v98
	v_fmac_f32_e32 v76, v98, v41
	v_add_f32_e32 v73, v73, v100
	v_fmac_f32_e32 v77, v100, v44
	v_add_f32_e32 v90, v90, v100
	v_fmac_f32_e32 v94, v100, v27
	v_add_f32_e32 v74, v74, v102
	v_fmac_f32_e32 v78, v102, v43
	v_add_f32_e32 v89, v89, v102
	v_fmac_f32_e32 v93, v102, v28
	v_add_f32_e32 v75, v75, v97
	v_fmac_f32_e32 v79, v97, v46
	v_add_f32_e32 v91, v91, v99
	v_fmac_f32_e32 v95, v99, v30
	v_add_f32_e32 v88, v88, v101
	v_fmac_f32_e32 v92, v101, v33
	v_add_f32_e32 v80, v80, v103
	v_fmac_f32_e32 v84, v103, v41
	v_sub_f32_e32 v96, v46, v45
	s_nop 0
	v_fma_f32 v96, -v96, v96, s20
	s_nop 0
	v_exp_f32_e32 v96, v96
	s_nop 0
	v_add_f32_e32 v81, v81, v108
	v_fmac_f32_e32 v85, v108, v44
	v_add_f32_e32 v90, v90, v108
	v_fmac_f32_e32 v94, v108, v35
	v_add_f32_e32 v82, v82, v110
	v_fmac_f32_e32 v86, v110, v43
	v_add_f32_e32 v89, v89, v110
	v_fmac_f32_e32 v93, v110, v36
	v_add_f32_e32 v83, v83, v105
	v_fmac_f32_e32 v87, v105, v46
	v_add_f32_e32 v91, v91, v107
	v_fmac_f32_e32 v95, v107, v38
	v_add_f32_e32 v88, v88, v109
	v_fmac_f32_e32 v92, v109, v41
	v_add_f32_e32 v89, v89, v111
	v_fmac_f32_e32 v93, v111, v44
	v_add_f32_e32 v90, v90, v111
	v_fmac_f32_e32 v94, v111, v43
	s_nop 0
	v_pk_add_f32 v[88:89], v[88:89], v[104:105] op_sel_hi:[1,0]
	v_pk_fma_f32 v[92:93], v[104:105], v[42:43], v[92:93] op_sel:[0,1,0] op_sel_hi:[0,0,1]
	v_pk_add_f32 v[90:91], v[90:91], v[106:107] op_sel_hi:[1,0]
	v_pk_fma_f32 v[94:95], v[106:107], v[44:45], v[94:95] op_sel:[0,1,0] op_sel_hi:[0,0,1]
	v_add_f32_e32 v91, v91, v96
	v_fmac_f32_e32 v95, v96, v46
	v_rcp_f32_e32 v96, v72
	v_rcp_f32_e32 v97, v73
	v_rcp_f32_e32 v98, v74
	v_rcp_f32_e32 v99, v75
	v_pk_mul_f32 v[76:77], v[76:77], s[34:35]
	v_pk_mul_f32 v[78:79], v[78:79], s[34:35]
	v_pk_mul_f32 v[76:77], v[76:77], v[96:97]
	v_pk_mul_f32 v[78:79], v[78:79], v[98:99]
	s_nop 0
	s_nop 0
	buffer_store_dwordx4 v[76:79], v114, s[12:15], 0 offen offset:2048 sc1
	s_waitcnt vmcnt(5)
	s_nop 0
	v_mov_b32_dpp v48, v52 row_shr:1 row_mask:0xf bank_mask:0xf
	v_mov_b32_dpp v49, v53 row_shr:1 row_mask:0xf bank_mask:0xf
	v_mov_b32_dpp v54, v50 row_shl:1 row_mask:0xf bank_mask:0xf
	v_mov_b32_dpp v55, v51 row_shl:1 row_mask:0xf bank_mask:0xf
	v_pk_mul_f32 v[50:51], v[50:51], s[32:33]
	v_pk_mul_f32 v[52:53], v[52:53], s[32:33]
	v_cndmask_b32_e64 v49, v49, v48, vcc
	v_cndmask_b32_e64 v54, v54, v55, s[16:17]
	v_pk_mul_f32 v[48:49], v[48:49], s[32:33]
	v_pk_mul_f32 v[54:55], v[54:55], s[32:33]
	s_setprio 0
	s_nop 0
	v_pk_add_f32 v[96:97], v[48:49], v[34:35] neg_lo:[0,1] neg_hi:[0,1]
	v_pk_add_f32 v[98:99], v[50:51], v[34:35] neg_lo:[0,1] neg_hi:[0,1]
	v_pk_add_f32 v[100:101], v[52:53], v[34:35] neg_lo:[0,1] neg_hi:[0,1]
	v_pk_add_f32 v[102:103], v[50:51], v[36:37] neg_lo:[0,1] neg_hi:[0,1]
	v_pk_fma_f32 v[96:97], v[96:97], v[96:97], s[28:29] neg_lo:[1,0,0] neg_hi:[1,0,0]
	v_pk_fma_f32 v[98:99], v[98:99], v[98:99], s[22:23] neg_lo:[1,0,0] neg_hi:[1,0,0]
	v_pk_fma_f32 v[100:101], v[100:101], v[100:101], s[28:29] neg_lo:[1,0,0] neg_hi:[1,0,0]
	v_pk_fma_f32 v[102:103], v[102:103], v[102:103], s[28:29] neg_lo:[1,0,0] neg_hi:[1,0,0]
	v_exp_f32_e32 v96, v96
	v_exp_f32_e32 v97, v97
	v_exp_f32_e32 v98, v98
	v_exp_f32_e32 v99, v99
	v_exp_f32_e32 v100, v100
	v_exp_f32_e32 v101, v101
	v_exp_f32_e32 v102, v102
	v_exp_f32_e32 v103, v103
	v_pk_add_f32 v[104:105], v[52:53], v[36:37] neg_lo:[0,1] neg_hi:[0,1]
	v_pk_add_f32 v[106:107], v[54:55], v[36:37] neg_lo:[0,1] neg_hi:[0,1]
	v_pk_add_f32 v[108:109], v[50:51], v[34:35] op_sel:[1,0] op_sel_hi:[0,1] neg_lo:[0,1] neg_hi:[0,1]
	v_pk_add_f32 v[110:111], v[52:53], v[36:37] op_sel:[1,0] op_sel_hi:[0,1] neg_lo:[0,1] neg_hi:[0,1]
	v_pk_fma_f32 v[104:105], v[104:105], v[104:105], s[22:23] neg_lo:[1,0,0] neg_hi:[1,0,0]
	v_pk_fma_f32 v[106:107], v[106:107], v[106:107], s[28:29] neg_lo:[1,0,0] neg_hi:[1,0,0]
	v_pk_fma_f32 v[108:109], v[108:109], v[108:109], s[26:27] neg_lo:[1,0,0] neg_hi:[1,0,0]
	v_pk_fma_f32 v[110:111], v[110:111], v[110:111], s[26:27] neg_lo:[1,0,0] neg_hi:[1,0,0]
	v_exp_f32_e32 v104, v104
	v_exp_f32_e32 v105, v105
	v_exp_f32_e32 v106, v106
	v_exp_f32_e32 v107, v107
	v_exp_f32_e32 v108, v108
	v_exp_f32_e32 v109, v109
	v_exp_f32_e32 v110, v110
	v_exp_f32_e32 v111, v111
	v_pk_add_f32 v[80:81], v[80:81], v[96:97]
	v_pk_fma_f32 v[84:85], v[96:97], v[48:49], v[84:85]
	v_pk_add_f32 v[82:83], v[82:83], v[102:103]
	v_pk_add_f32 v[80:81], v[80:81], v[98:99]
	v_pk_fma_f32 v[84:85], v[98:99], v[50:51], v[84:85]
	v_pk_fma_f32 v[86:87], v[102:103], v[50:51], v[86:87]
	v_pk_add_f32 v[80:81], v[80:81], v[100:101]
	v_pk_fma_f32 v[84:85], v[100:101], v[52:53], v[84:85]
	v_pk_add_f32 v[96:97], v[48:49], v[42:43] neg_lo:[0,1] neg_hi:[0,1]
	v_pk_add_f32 v[98:99], v[50:51], v[42:43] neg_lo:[0,1] neg_hi:[0,1]
	v_pk_add_f32 v[100:101], v[52:53], v[42:43] neg_lo:[0,1] neg_hi:[0,1]
	v_pk_add_f32 v[102:103], v[50:51], v[44:45] neg_lo:[0,1] neg_hi:[0,1]
	v_pk_fma_f32 v[96:97], v[96:97], v[96:97], s[26:27] neg_lo:[1,0,0] neg_hi:[1,0,0]
	v_pk_fma_f32 v[98:99], v[98:99], v[98:99], s[20:21] neg_lo:[1,0,0] neg_hi:[1,0,0]
	v_pk_fma_f32 v[100:101], v[100:101], v[100:101], s[26:27] neg_lo:[1,0,0] neg_hi:[1,0,0]
	v_pk_fma_f32 v[102:103], v[102:103], v[102:103], s[26:27] neg_lo:[1,0,0] neg_hi:[1,0,0]
	v_exp_f32_e32 v96, v96
	v_exp_f32_e32 v97, v97
	v_exp_f32_e32 v98, v98
	v_exp_f32_e32 v99, v99
	v_exp_f32_e32 v100, v100
	v_exp_f32_e32 v101, v101
	v_exp_f32_e32 v102, v102
	v_exp_f32_e32 v103, v103
	v_pk_add_f32 v[82:83], v[82:83], v[104:105]
	v_pk_fma_f32 v[86:87], v[104:105], v[52:53], v[86:87]
	v_pk_add_f32 v[80:81], v[80:81], v[108:109]
	v_pk_add_f32 v[82:83], v[82:83], v[106:107]
	v_pk_fma_f32 v[86:87], v[106:107], v[54:55], v[86:87]
	v_pk_fma_f32 v[84:85], v[108:109], v[50:51], v[84:85] op_sel:[0,1,0] op_sel_hi:[1,0,1]
	v_pk_add_f32 v[82:83], v[82:83], v[110:111]
	v_pk_fma_f32 v[86:87], v[110:111], v[52:53], v[86:87] op_sel:[0,1,0] op_sel_hi:[1,0,1]
	v_pk_add_f32 v[104:105], v[52:53], v[44:45] neg_lo:[0,1] neg_hi:[0,1]
	v_pk_add_f32 v[106:107], v[54:55], v[44:45] neg_lo:[0,1] neg_hi:[0,1]
	v_pk_add_f32 v[108:109], v[50:51], v[42:43] op_sel:[1,0] op_sel_hi:[0,1] neg_lo:[0,1] neg_hi:[0,1]
	v_pk_add_f32 v[110:111], v[52:53], v[44:45] op_sel:[1,0] op_sel_hi:[0,1] neg_lo:[0,1] neg_hi:[0,1]
	v_pk_fma_f32 v[104:105], v[104:105], v[104:105], s[20:21] neg_lo:[1,0,0] neg_hi:[1,0,0]
	v_pk_fma_f32 v[106:107], v[106:107], v[106:107], s[26:27] neg_lo:[1,0,0] neg_hi:[1,0,0]
	v_pk_fma_f32 v[108:109], v[108:109], v[108:109], s[24:25] neg_lo:[1,0,0] neg_hi:[1,0,0]
	v_pk_fma_f32 v[110:111], v[110:111], v[110:111], s[24:25] neg_lo:[1,0,0] neg_hi:[1,0,0]
	v_exp_f32_e32 v104, v104
	v_exp_f32_e32 v105, v105
	v_exp_f32_e32 v106, v106
	v_exp_f32_e32 v107, v107
	v_exp_f32_e32 v108, v108
	v_exp_f32_e32 v109, v109
	v_exp_f32_e32 v110, v110
	v_exp_f32_e32 v111, v111
	v_pk_add_f32 v[88:89], v[88:89], v[96:97]
	v_pk_fma_f32 v[92:93], v[96:97], v[48:49], v[92:93]
	v_pk_add_f32 v[90:91], v[90:91], v[102:103]
	v_pk_add_f32 v[88:89], v[88:89], v[98:99]
	v_pk_fma_f32 v[92:93], v[98:99], v[50:51], v[92:93]
	v_pk_fma_f32 v[94:95], v[102:103], v[50:51], v[94:95]
	v_pk_add_f32 v[88:89], v[88:89], v[100:101]
	v_pk_fma_f32 v[92:93], v[100:101], v[52:53], v[92:93]
	v_sub_f32_e32 v96, v49, v34
	v_sub_f32_e32 v98, v52, v35
	v_sub_f32_e32 v100, v51, v36
	v_sub_f32_e32 v102, v54, v37
	v_sub_f32_e32 v97, v49, v42
	v_sub_f32_e32 v99, v52, v43
	v_sub_f32_e32 v101, v51, v44
	v_sub_f32_e32 v103, v54, v45
	v_fma_f32 v96, -v96, v96, s26
	v_fma_f32 v98, -v98, v98, s26
	v_fma_f32 v100, -v100, v100, s26
	v_fma_f32 v102, -v102, v102, s26
	v_fma_f32 v97, -v97, v97, s24
	v_fma_f32 v99, -v99, v99, s24
	v_fma_f32 v101, -v101, v101, s24
	v_fma_f32 v103, -v103, v103, s24
	v_exp_f32_e32 v96, v96
	v_exp_f32_e32 v98, v98
	v_exp_f32_e32 v100, v100
	v_exp_f32_e32 v102, v102
	v_exp_f32_e32 v97, v97
	v_exp_f32_e32 v99, v99
	v_exp_f32_e32 v101, v101
	v_exp_f32_e32 v103, v103
	v_pk_add_f32 v[90:91], v[90:91], v[104:105]
	v_pk_fma_f32 v[94:95], v[104:105], v[52:53], v[94:95]
	v_pk_add_f32 v[88:89], v[88:89], v[108:109]
	v_pk_add_f32 v[90:91], v[90:91], v[106:107]
	v_pk_fma_f32 v[94:95], v[106:107], v[54:55], v[94:95]
	v_pk_fma_f32 v[92:93], v[108:109], v[50:51], v[92:93] op_sel:[0,1,0] op_sel_hi:[1,0,1]
	v_pk_add_f32 v[90:91], v[90:91], v[110:111]
	v_pk_fma_f32 v[94:95], v[110:111], v[52:53], v[94:95] op_sel:[0,1,0] op_sel_hi:[1,0,1]
	v_add_f32_e32 v80, v80, v96
	v_fmac_f32_e32 v84, v96, v49
	v_add_f32_e32 v81, v81, v98
	v_fmac_f32_e32 v85, v98, v52
	v_add_f32_e32 v82, v82, v100
	v_fmac_f32_e32 v86, v100, v51
	v_add_f32_e32 v83, v83, v102
	v_fmac_f32_e32 v87, v102, v54
	v_add_f32_e32 v88, v88, v97
	v_fmac_f32_e32 v92, v97, v49
	v_add_f32_e32 v89, v89, v99
	v_fmac_f32_e32 v93, v99, v52
	v_add_f32_e32 v90, v90, v101
	v_fmac_f32_e32 v94, v101, v51
	v_add_f32_e32 v91, v91, v103
	v_fmac_f32_e32 v95, v103, v54
	v_rcp_f32_e32 v96, v80
	v_rcp_f32_e32 v97, v81
	v_rcp_f32_e32 v98, v82
	v_rcp_f32_e32 v99, v83
	v_pk_mul_f32 v[84:85], v[84:85], s[34:35]
	v_pk_mul_f32 v[86:87], v[86:87], s[34:35]
	v_pk_mul_f32 v[84:85], v[84:85], v[96:97]
	v_pk_mul_f32 v[86:87], v[86:87], v[98:99]
	s_nop 0
	s_nop 0
	buffer_store_dwordx4 v[84:87], v119, s[12:15], 0 offen sc1
	s_waitcnt vmcnt(3)
	s_nop 0
	v_mov_b32_dpp v56, v60 row_shr:1 row_mask:0xf bank_mask:0xf
	v_mov_b32_dpp v57, v61 row_shr:1 row_mask:0xf bank_mask:0xf
	v_mov_b32_dpp v62, v58 row_shl:1 row_mask:0xf bank_mask:0xf
	v_mov_b32_dpp v63, v59 row_shl:1 row_mask:0xf bank_mask:0xf
	v_pk_mul_f32 v[58:59], v[58:59], s[32:33]
	v_pk_mul_f32 v[60:61], v[60:61], s[32:33]
	v_cndmask_b32_e64 v57, v57, v56, vcc
	v_cndmask_b32_e64 v62, v62, v63, s[16:17]
	v_pk_mul_f32 v[56:57], v[56:57], s[32:33]
	v_pk_mul_f32 v[62:63], v[62:63], s[32:33]
	s_setprio 0
	s_nop 0
	v_pk_add_f32 v[96:97], v[56:57], v[42:43] neg_lo:[0,1] neg_hi:[0,1]
	v_pk_add_f32 v[98:99], v[58:59], v[42:43] neg_lo:[0,1] neg_hi:[0,1]
	v_pk_add_f32 v[100:101], v[60:61], v[42:43] neg_lo:[0,1] neg_hi:[0,1]
	v_pk_add_f32 v[102:103], v[58:59], v[44:45] neg_lo:[0,1] neg_hi:[0,1]
	v_pk_fma_f32 v[96:97], v[96:97], v[96:97], s[28:29] neg_lo:[1,0,0] neg_hi:[1,0,0]
	v_pk_fma_f32 v[98:99], v[98:99], v[98:99], s[22:23] neg_lo:[1,0,0] neg_hi:[1,0,0]
	v_pk_fma_f32 v[100:101], v[100:101], v[100:101], s[28:29] neg_lo:[1,0,0] neg_hi:[1,0,0]
	v_pk_fma_f32 v[102:103], v[102:103], v[102:103], s[28:29] neg_lo:[1,0,0] neg_hi:[1,0,0]
	v_exp_f32_e32 v96, v96
	v_exp_f32_e32 v97, v97
	v_exp_f32_e32 v98, v98
	v_exp_f32_e32 v99, v99
	v_exp_f32_e32 v100, v100
	v_exp_f32_e32 v101, v101
	v_exp_f32_e32 v102, v102
	v_exp_f32_e32 v103, v103
	v_pk_add_f32 v[104:105], v[60:61], v[44:45] neg_lo:[0,1] neg_hi:[0,1]
	v_pk_add_f32 v[106:107], v[62:63], v[44:45] neg_lo:[0,1] neg_hi:[0,1]
	v_pk_add_f32 v[108:109], v[58:59], v[42:43] op_sel:[1,0] op_sel_hi:[0,1] neg_lo:[0,1] neg_hi:[0,1]
	v_pk_add_f32 v[110:111], v[60:61], v[44:45] op_sel:[1,0] op_sel_hi:[0,1] neg_lo:[0,1] neg_hi:[0,1]
	v_pk_fma_f32 v[104:105], v[104:105], v[104:105], s[22:23] neg_lo:[1,0,0] neg_hi:[1,0,0]
	v_pk_fma_f32 v[106:107], v[106:107], v[106:107], s[28:29] neg_lo:[1,0,0] neg_hi:[1,0,0]
	v_pk_fma_f32 v[108:109], v[108:109], v[108:109], s[26:27] neg_lo:[1,0,0] neg_hi:[1,0,0]
	v_pk_fma_f32 v[110:111], v[110:111], v[110:111], s[26:27] neg_lo:[1,0,0] neg_hi:[1,0,0]
	v_exp_f32_e32 v104, v104
	v_exp_f32_e32 v105, v105
	v_exp_f32_e32 v106, v106
	v_exp_f32_e32 v107, v107
	v_exp_f32_e32 v108, v108
	v_exp_f32_e32 v109, v109
	v_exp_f32_e32 v110, v110
	v_exp_f32_e32 v111, v111
	v_pk_add_f32 v[88:89], v[88:89], v[96:97]
	v_pk_fma_f32 v[92:93], v[96:97], v[56:57], v[92:93]
	v_pk_add_f32 v[90:91], v[90:91], v[102:103]
	v_pk_add_f32 v[88:89], v[88:89], v[98:99]
	v_pk_fma_f32 v[92:93], v[98:99], v[58:59], v[92:93]
	v_pk_fma_f32 v[94:95], v[102:103], v[58:59], v[94:95]
	v_pk_add_f32 v[88:89], v[88:89], v[100:101]
	v_pk_fma_f32 v[92:93], v[100:101], v[60:61], v[92:93]
	v_sub_f32_e32 v96, v57, v42
	v_sub_f32_e32 v98, v60, v43
	v_sub_f32_e32 v100, v59, v44
	v_sub_f32_e32 v102, v62, v45
	v_fma_f32 v96, -v96, v96, s26
	v_fma_f32 v98, -v98, v98, s26
	v_fma_f32 v100, -v100, v100, s26
	v_fma_f32 v102, -v102, v102, s26
	v_exp_f32_e32 v96, v96
	v_exp_f32_e32 v98, v98
	v_exp_f32_e32 v100, v100
	v_exp_f32_e32 v102, v102
	v_pk_add_f32 v[90:91], v[90:91], v[104:105]
	v_pk_fma_f32 v[94:95], v[104:105], v[60:61], v[94:95]
	v_pk_add_f32 v[88:89], v[88:89], v[108:109]
	v_pk_add_f32 v[90:91], v[90:91], v[106:107]
	v_pk_fma_f32 v[94:95], v[106:107], v[62:63], v[94:95]
	v_pk_fma_f32 v[92:93], v[108:109], v[58:59], v[92:93] op_sel:[0,1,0] op_sel_hi:[1,0,1]
	v_pk_add_f32 v[90:91], v[90:91], v[110:111]
	v_pk_fma_f32 v[94:95], v[110:111], v[60:61], v[94:95] op_sel:[0,1,0] op_sel_hi:[1,0,1]
	v_add_f32_e32 v88, v88, v96
	v_fmac_f32_e32 v92, v96, v57
	v_add_f32_e32 v89, v89, v98
	v_fmac_f32_e32 v93, v98, v60
	v_add_f32_e32 v90, v90, v100
	v_fmac_f32_e32 v94, v100, v59
	v_add_f32_e32 v91, v91, v102
	v_fmac_f32_e32 v95, v102, v62
	v_rcp_f32_e32 v96, v88
	v_rcp_f32_e32 v97, v89
	v_rcp_f32_e32 v98, v90
	v_rcp_f32_e32 v99, v91
	v_pk_mul_f32 v[92:93], v[92:93], s[34:35]
	v_pk_mul_f32 v[94:95], v[94:95], s[34:35]
	v_pk_mul_f32 v[92:93], v[92:93], v[96:97]
	v_pk_mul_f32 v[94:95], v[94:95], v[98:99]
	s_nop 0
	s_nop 0
	buffer_store_dwordx4 v[92:95], v119, s[12:15], 0 offen offset:2048 sc1
	s_endpgm

	.amdhsa_kernel _Z16bilateral_kernelPKfS0_Pf
		.amdhsa_group_segment_fixed_size 0
		.amdhsa_private_segment_fixed_size 0
		.amdhsa_kernarg_size 24
		.amdhsa_user_sgpr_count 2
		.amdhsa_user_sgpr_dispatch_ptr 0
		.amdhsa_user_sgpr_queue_ptr 0
		.amdhsa_user_sgpr_kernarg_segment_ptr 1
		.amdhsa_user_sgpr_dispatch_id 0
		.amdhsa_user_sgpr_kernarg_preload_length 0
		.amdhsa_user_sgpr_kernarg_preload_offset 0
		.amdhsa_user_sgpr_private_segment_size 0
		.amdhsa_uses_dynamic_stack 0
		.amdhsa_enable_private_segment 0
		.amdhsa_system_sgpr_workgroup_id_x 1
		.amdhsa_system_sgpr_workgroup_id_y 0
		.amdhsa_system_sgpr_workgroup_id_z 0
		.amdhsa_system_sgpr_workgroup_info 0
		.amdhsa_system_vgpr_workitem_id 0
		.amdhsa_next_free_vgpr 128
		.amdhsa_next_free_sgpr 40
		.amdhsa_accum_offset 128
		.amdhsa_reserve_vcc 1
		.amdhsa_float_round_mode_32 0
		.amdhsa_float_round_mode_16_64 0
		.amdhsa_float_denorm_mode_32 3
		.amdhsa_float_denorm_mode_16_64 3
		.amdhsa_dx10_clamp 1
		.amdhsa_ieee_mode 1
		.amdhsa_fp16_overflow 0
		.amdhsa_tg_split 0
		.amdhsa_exception_fp_ieee_invalid_op 0
		.amdhsa_exception_fp_denorm_src 0
		.amdhsa_exception_fp_ieee_div_zero 0
		.amdhsa_exception_fp_ieee_overflow 0
		.amdhsa_exception_fp_ieee_underflow 0
		.amdhsa_exception_fp_ieee_inexact 0
		.amdhsa_exception_int_div_zero 0
	.end_amdhsa_kernel

amdhsa.kernels:
  - .agpr_count:     0
    .args:
      - .actual_access:  read_only
        .address_space:  global
        .offset:         0
        .size:           8
        .value_kind:     global_buffer
      - .actual_access:  read_only
        .address_space:  global
        .offset:         8
        .size:           8
        .value_kind:     global_buffer
      - .actual_access:  write_only
        .address_space:  global
        .offset:         16
        .size:           8
        .value_kind:     global_buffer
    .group_segment_fixed_size: 0
    .kernarg_segment_align: 8
    .kernarg_segment_size: 24
    .language:       OpenCL C
    .language_version:
      - 2
      - 0
    .max_flat_workgroup_size: 256
    .name:           _Z16bilateral_kernelPKfS0_Pf
    .private_segment_fixed_size: 0
    .sgpr_count:     46
    .sgpr_spill_count: 0
    .symbol:         _Z16bilateral_kernelPKfS0_Pf.kd
    .uniform_work_group_size: 1
    .uses_dynamic_stack: false
    .vgpr_count:     128
    .vgpr_spill_count: 0
    .wavefront_size: 64
